# qkv prologue and K loop hand-written with BK=64 full-line LDS-DMA and a single swizzled 40KB stage; fixup V recompute on two MFMA chains with deep prefetch
# speedup vs baseline: 1.0540x; 1.0540x over previous
_Z14k_qkv_temporalPKDF16_S0_PKfPDF16_S3_S3_PfPi:
	s_load_dwordx4 s[36:39], s[0:1], 0x0
	s_load_dwordx2 s[40:41], s[0:1], 0x10
	s_load_dwordx4 s[8:11], s[0:1], 0x30
	s_and_b32 s3, s2, 7
	s_mul_i32 s3, s3, 0x71
	s_lshr_b32 s4, s2, 3
	s_add_u32 s3, s3, s4
	s_and_b32 s22, s3, 7
	s_lshr_b32 s16, s3, 3
	s_mul_i32 s16, s16, 14
	v_lshrrev_b32_e32 v1, 6, v0
	v_and_b32_e32 v92, 15, v0
	v_bfe_u32 v90, v0, 4, 2
	v_lshlrev_b32_e32 v95, 2, v90
	v_lshl_or_b32 v91, v1, 5, v95
	v_bfe_u32 v162, v0, 3, 3
	v_and_b32_e32 v163, 7, v0
	v_lshrrev_b32_e32 v110, 1, v162
	v_and_b32_e32 v111, 1, v1
	v_lshl_or_b32 v110, v111, 2, v110
	v_xor_b32_e32 v110, v163, v110
	v_lshlrev_b32_e32 v110, 4, v110
	v_lshl_or_b32 v111, v1, 3, v162
	s_mov_b32 s42, 0x12492493
	s_movk_i32 s43, 0x627
	s_movk_i32 s44, 0x628
	v_add_u32_e32 v112, 0, v111
	v_min_u32_e32 v112, 0x7d, v112
	v_mul_hi_u32 v113, v112, s42
	v_mul_u32_u24_e32 v114, 14, v113
	v_sub_u32_e32 v114, v112, v114
	v_add_u32_e32 v114, s16, v114
	v_min_u32_e32 v114, s43, v114
	v_mad_u32_u24 v114, v113, s44, v114
	v_lshl_or_b32 v100, v114, 10, v110
	v_add_u32_e32 v112, 32, v111
	v_min_u32_e32 v112, 0x7d, v112
	v_mul_hi_u32 v113, v112, s42
	v_mul_u32_u24_e32 v114, 14, v113
	v_sub_u32_e32 v114, v112, v114
	v_add_u32_e32 v114, s16, v114
	v_min_u32_e32 v114, s43, v114
	v_mad_u32_u24 v114, v113, s44, v114
	v_lshl_or_b32 v101, v114, 10, v110
	v_add_u32_e32 v112, 64, v111
	v_min_u32_e32 v112, 0x7d, v112
	v_mul_hi_u32 v113, v112, s42
	v_mul_u32_u24_e32 v114, 14, v113
	v_sub_u32_e32 v114, v112, v114
	v_add_u32_e32 v114, s16, v114
	v_min_u32_e32 v114, s43, v114
	v_mad_u32_u24 v114, v113, s44, v114
	v_lshl_or_b32 v102, v114, 10, v110
	v_add_u32_e32 v112, 96, v111
	v_min_u32_e32 v112, 0x7d, v112
	v_mul_hi_u32 v113, v112, s42
	v_mul_u32_u24_e32 v114, 14, v113
	v_sub_u32_e32 v114, v112, v114
	v_add_u32_e32 v114, s16, v114
	v_min_u32_e32 v114, s43, v114
	v_mad_u32_u24 v114, v113, s44, v114
	v_lshl_or_b32 v103, v114, 10, v110
	s_lshl_b32 s45, s22, 6
	v_add_u32_e32 v112, s45, v111
	v_lshl_or_b32 v112, v112, 10, v110
	v_mov_b32_e32 v104, v112
	v_add_u32_e32 v105, 0x8000, v112
	v_add_u32_e32 v106, 0x80000, v112
	v_add_u32_e32 v107, 0x88000, v112
	v_add_u32_e32 v108, 0x100000, v112
	v_add_u32_e32 v109, 0x108000, v112
	v_lshlrev_b32_e32 v113, 10, v1
	s_nop 0
	v_readfirstlane_b32 s24, v113
	s_add_u32 s25, s24, 0x1000
	s_add_u32 s26, s24, 0x2000
	s_add_u32 s27, s24, 0x3000
	s_add_u32 s28, s24, 0x4000
	s_add_u32 s29, s24, 0x5000
	s_add_u32 s30, s24, 0x6000
	s_add_u32 s31, s24, 0x7000
	s_add_u32 s32, s24, 0x8000
	s_add_u32 s33, s24, 0x9000
	v_lshrrev_b32_e32 v113, 1, v92
	v_xor_b32_e32 v113, v90, v113
	v_lshlrev_b32_e32 v113, 4, v113
	v_lshl_or_b32 v160, v92, 7, v113
	v_xor_b32_e32 v161, 64, v160
	v_lshlrev_b32_e32 v114, 12, v1
	v_add_u32_e32 v158, v114, v160
	v_xor_b32_e32 v159, 64, v158
	v_lshl_add_u32 v114, s22, 6, v92
	v_lshlrev_b32_e32 v114, 2, v114
	v_add_u32_e32 v115, 0x1000, v114
	s_waitcnt lgkmcnt(0)
	global_load_dword v116, v114, s[40:41] offset:0
	global_load_dword v117, v114, s[40:41] offset:64
	global_load_dword v118, v114, s[40:41] offset:128
	global_load_dword v119, v114, s[40:41] offset:192
	global_load_dword v120, v114, s[40:41] offset:2048
	global_load_dword v121, v114, s[40:41] offset:2112
	global_load_dword v122, v114, s[40:41] offset:2176
	global_load_dword v123, v114, s[40:41] offset:2240
	global_load_dword v124, v115, s[40:41] offset:0
	global_load_dword v125, v115, s[40:41] offset:64
	global_load_dword v126, v115, s[40:41] offset:128
	global_load_dword v127, v115, s[40:41] offset:192
	s_mov_b32 m0, s24
	s_nop 0
	global_load_lds_dwordx4 v100, s[36:37]
	s_mov_b32 m0, s25
	s_nop 0
	global_load_lds_dwordx4 v101, s[36:37]
	s_mov_b32 m0, s26
	s_nop 0
	global_load_lds_dwordx4 v102, s[36:37]
	s_mov_b32 m0, s27
	s_nop 0
	global_load_lds_dwordx4 v103, s[36:37]
	s_mov_b32 m0, s28
	s_nop 0
	global_load_lds_dwordx4 v104, s[38:39]
	s_mov_b32 m0, s29
	s_nop 0
	global_load_lds_dwordx4 v105, s[38:39]
	s_mov_b32 m0, s30
	s_nop 0
	global_load_lds_dwordx4 v106, s[38:39]
	s_mov_b32 m0, s31
	s_nop 0
	global_load_lds_dwordx4 v107, s[38:39]
	s_mov_b32 m0, s32
	s_nop 0
	global_load_lds_dwordx4 v108, s[38:39]
	s_mov_b32 m0, s33
	s_nop 0
	global_load_lds_dwordx4 v109, s[38:39]
	s_add_u32 s36, s36, 0x80
	s_addc_u32 s37, s37, 0
	s_add_u32 s38, s38, 0x80
	s_addc_u32 s39, s39, 0
	s_waitcnt vmcnt(10)
	v_mov_b32_e32 v164, v116
	v_mov_b32_e32 v165, v116
	v_mov_b32_e32 v166, v116
	v_mov_b32_e32 v167, v116
	v_mov_b32_e32 v62, v116
	v_mov_b32_e32 v63, v116
	v_mov_b32_e32 v64, v116
	v_mov_b32_e32 v65, v116
	v_mov_b32_e32 v86, v117
	v_mov_b32_e32 v87, v117
	v_mov_b32_e32 v88, v117
	v_mov_b32_e32 v89, v117
	v_mov_b32_e32 v58, v117
	v_mov_b32_e32 v59, v117
	v_mov_b32_e32 v60, v117
	v_mov_b32_e32 v61, v117
	v_mov_b32_e32 v96, v118
	v_mov_b32_e32 v97, v118
	v_mov_b32_e32 v98, v118
	v_mov_b32_e32 v99, v118
	v_mov_b32_e32 v54, v118
	v_mov_b32_e32 v55, v118
	v_mov_b32_e32 v56, v118
	v_mov_b32_e32 v57, v118
	v_mov_b32_e32 v82, v119
	v_mov_b32_e32 v83, v119
	v_mov_b32_e32 v84, v119
	v_mov_b32_e32 v85, v119
	v_mov_b32_e32 v50, v119
	v_mov_b32_e32 v51, v119
	v_mov_b32_e32 v52, v119
	v_mov_b32_e32 v53, v119
	v_mov_b32_e32 v78, v120
	v_mov_b32_e32 v79, v120
	v_mov_b32_e32 v80, v120
	v_mov_b32_e32 v81, v120
	v_mov_b32_e32 v46, v120
	v_mov_b32_e32 v47, v120
	v_mov_b32_e32 v48, v120
	v_mov_b32_e32 v49, v120
	v_mov_b32_e32 v74, v121
	v_mov_b32_e32 v75, v121
	v_mov_b32_e32 v76, v121
	v_mov_b32_e32 v77, v121
	v_mov_b32_e32 v42, v121
	v_mov_b32_e32 v43, v121
	v_mov_b32_e32 v44, v121
	v_mov_b32_e32 v45, v121
	v_mov_b32_e32 v70, v122
	v_mov_b32_e32 v71, v122
	v_mov_b32_e32 v72, v122
	v_mov_b32_e32 v73, v122
	v_mov_b32_e32 v38, v122
	v_mov_b32_e32 v39, v122
	v_mov_b32_e32 v40, v122
	v_mov_b32_e32 v41, v122
	v_mov_b32_e32 v66, v123
	v_mov_b32_e32 v67, v123
	v_mov_b32_e32 v68, v123
	v_mov_b32_e32 v69, v123
	v_mov_b32_e32 v34, v123
	v_mov_b32_e32 v35, v123
	v_mov_b32_e32 v36, v123
	v_mov_b32_e32 v37, v123
	v_mov_b32_e32 v18, v124
	v_mov_b32_e32 v19, v124
	v_mov_b32_e32 v20, v124
	v_mov_b32_e32 v21, v124
	v_mov_b32_e32 v2, v124
	v_mov_b32_e32 v3, v124
	v_mov_b32_e32 v4, v124
	v_mov_b32_e32 v5, v124
	v_mov_b32_e32 v26, v125
	v_mov_b32_e32 v27, v125
	v_mov_b32_e32 v28, v125
	v_mov_b32_e32 v29, v125
	v_mov_b32_e32 v10, v125
	v_mov_b32_e32 v11, v125
	v_mov_b32_e32 v12, v125
	v_mov_b32_e32 v13, v125
	v_mov_b32_e32 v22, v126
	v_mov_b32_e32 v23, v126
	v_mov_b32_e32 v24, v126
	v_mov_b32_e32 v25, v126
	v_mov_b32_e32 v6, v126
	v_mov_b32_e32 v7, v126
	v_mov_b32_e32 v8, v126
	v_mov_b32_e32 v9, v126
	v_mov_b32_e32 v30, v127
	v_mov_b32_e32 v31, v127
	v_mov_b32_e32 v32, v127
	v_mov_b32_e32 v33, v127
	v_mov_b32_e32 v14, v127
	v_mov_b32_e32 v15, v127
	v_mov_b32_e32 v16, v127
	v_mov_b32_e32 v17, v127
	s_waitcnt vmcnt(0)
	s_barrier
	ds_read_b128 v[110:113], v158 offset:0
	ds_read_b128 v[114:117], v158 offset:2048
	ds_read_b128 v[118:121], v159 offset:0
	ds_read_b128 v[122:125], v159 offset:2048
	ds_read_b128 v[126:129], v160 offset:16384
	ds_read_b128 v[130:133], v160 offset:18432
	ds_read_b128 v[134:137], v160 offset:20480
	ds_read_b128 v[138:141], v160 offset:22528
	ds_read_b128 v[142:145], v160 offset:24576
	ds_read_b128 v[146:149], v160 offset:26624
	ds_read_b128 v[150:153], v160 offset:28672
	ds_read_b128 v[154:157], v160 offset:30720
	s_waitcnt lgkmcnt(7)
	v_mfma_f32_16x16x32_f16 v[164:167], v[110:113], v[126:129], v[164:167]
	v_mfma_f32_16x16x32_f16 v[62:65], v[114:117], v[126:129], v[62:65]
	ds_read_b128 v[126:129], v160 offset:32768
	s_waitcnt lgkmcnt(7)
	v_mfma_f32_16x16x32_f16 v[86:89], v[110:113], v[130:133], v[86:89]
	v_mfma_f32_16x16x32_f16 v[58:61], v[114:117], v[130:133], v[58:61]
	ds_read_b128 v[130:133], v160 offset:34816
	s_waitcnt lgkmcnt(7)
	v_mfma_f32_16x16x32_f16 v[96:99], v[110:113], v[134:137], v[96:99]
	v_mfma_f32_16x16x32_f16 v[54:57], v[114:117], v[134:137], v[54:57]
	ds_read_b128 v[134:137], v160 offset:36864
	s_waitcnt lgkmcnt(7)
	v_mfma_f32_16x16x32_f16 v[82:85], v[110:113], v[138:141], v[82:85]
	v_mfma_f32_16x16x32_f16 v[50:53], v[114:117], v[138:141], v[50:53]
	ds_read_b128 v[138:141], v160 offset:38912
	s_waitcnt lgkmcnt(7)
	v_mfma_f32_16x16x32_f16 v[78:81], v[110:113], v[142:145], v[78:81]
	v_mfma_f32_16x16x32_f16 v[46:49], v[114:117], v[142:145], v[46:49]
	ds_read_b128 v[142:145], v161 offset:16384
	s_waitcnt lgkmcnt(7)
	v_mfma_f32_16x16x32_f16 v[74:77], v[110:113], v[146:149], v[74:77]
	v_mfma_f32_16x16x32_f16 v[42:45], v[114:117], v[146:149], v[42:45]
	ds_read_b128 v[146:149], v161 offset:18432
	s_waitcnt lgkmcnt(7)
	v_mfma_f32_16x16x32_f16 v[70:73], v[110:113], v[150:153], v[70:73]
	v_mfma_f32_16x16x32_f16 v[38:41], v[114:117], v[150:153], v[38:41]
	ds_read_b128 v[150:153], v161 offset:20480
	s_waitcnt lgkmcnt(7)
	v_mfma_f32_16x16x32_f16 v[66:69], v[110:113], v[154:157], v[66:69]
	v_mfma_f32_16x16x32_f16 v[34:37], v[114:117], v[154:157], v[34:37]
	ds_read_b128 v[154:157], v161 offset:22528
	s_waitcnt lgkmcnt(7)
	v_mfma_f32_16x16x32_f16 v[18:21], v[110:113], v[126:129], v[18:21]
	v_mfma_f32_16x16x32_f16 v[2:5], v[114:117], v[126:129], v[2:5]
	ds_read_b128 v[126:129], v161 offset:24576
	s_waitcnt lgkmcnt(7)
	v_mfma_f32_16x16x32_f16 v[26:29], v[110:113], v[130:133], v[26:29]
	v_mfma_f32_16x16x32_f16 v[10:13], v[114:117], v[130:133], v[10:13]
	ds_read_b128 v[130:133], v161 offset:26624
	s_waitcnt lgkmcnt(7)
	v_mfma_f32_16x16x32_f16 v[22:25], v[110:113], v[134:137], v[22:25]
	v_mfma_f32_16x16x32_f16 v[6:9], v[114:117], v[134:137], v[6:9]
	ds_read_b128 v[134:137], v161 offset:28672
	s_waitcnt lgkmcnt(7)
	v_mfma_f32_16x16x32_f16 v[30:33], v[110:113], v[138:141], v[30:33]
	v_mfma_f32_16x16x32_f16 v[14:17], v[114:117], v[138:141], v[14:17]
	ds_read_b128 v[138:141], v161 offset:30720
	s_waitcnt lgkmcnt(7)
	v_mfma_f32_16x16x32_f16 v[164:167], v[118:121], v[142:145], v[164:167]
	v_mfma_f32_16x16x32_f16 v[62:65], v[122:125], v[142:145], v[62:65]
	ds_read_b128 v[142:145], v161 offset:32768
	s_waitcnt lgkmcnt(7)
	v_mfma_f32_16x16x32_f16 v[86:89], v[118:121], v[146:149], v[86:89]
	v_mfma_f32_16x16x32_f16 v[58:61], v[122:125], v[146:149], v[58:61]
	ds_read_b128 v[146:149], v161 offset:34816
	s_waitcnt lgkmcnt(7)
	v_mfma_f32_16x16x32_f16 v[96:99], v[118:121], v[150:153], v[96:99]
	v_mfma_f32_16x16x32_f16 v[54:57], v[122:125], v[150:153], v[54:57]
	ds_read_b128 v[150:153], v161 offset:36864
	s_waitcnt lgkmcnt(7)
	v_mfma_f32_16x16x32_f16 v[82:85], v[118:121], v[154:157], v[82:85]
	v_mfma_f32_16x16x32_f16 v[50:53], v[122:125], v[154:157], v[50:53]
	ds_read_b128 v[154:157], v161 offset:38912
	s_waitcnt lgkmcnt(0)
	s_barrier
	s_mov_b32 m0, s24
	s_nop 0
	global_load_lds_dwordx4 v100, s[36:37]
	s_mov_b32 m0, s25
	s_nop 0
	global_load_lds_dwordx4 v101, s[36:37]
	s_mov_b32 m0, s26
	s_nop 0
	global_load_lds_dwordx4 v102, s[36:37]
	s_mov_b32 m0, s27
	s_nop 0
	global_load_lds_dwordx4 v103, s[36:37]
	s_mov_b32 m0, s28
	s_nop 0
	global_load_lds_dwordx4 v104, s[38:39]
	s_mov_b32 m0, s29
	s_nop 0
	global_load_lds_dwordx4 v105, s[38:39]
	s_mov_b32 m0, s30
	s_nop 0
	global_load_lds_dwordx4 v106, s[38:39]
	s_mov_b32 m0, s31
	s_nop 0
	global_load_lds_dwordx4 v107, s[38:39]
	s_mov_b32 m0, s32
	s_nop 0
	global_load_lds_dwordx4 v108, s[38:39]
	s_mov_b32 m0, s33
	s_nop 0
	global_load_lds_dwordx4 v109, s[38:39]
	s_add_u32 s36, s36, 0x80
	s_addc_u32 s37, s37, 0
	s_add_u32 s38, s38, 0x80
	s_addc_u32 s39, s39, 0
	s_waitcnt lgkmcnt(7)
	v_mfma_f32_16x16x32_f16 v[78:81], v[118:121], v[126:129], v[78:81]
	v_mfma_f32_16x16x32_f16 v[46:49], v[122:125], v[126:129], v[46:49]
	s_waitcnt lgkmcnt(6)
	v_mfma_f32_16x16x32_f16 v[74:77], v[118:121], v[130:133], v[74:77]
	v_mfma_f32_16x16x32_f16 v[42:45], v[122:125], v[130:133], v[42:45]
	s_waitcnt lgkmcnt(5)
	v_mfma_f32_16x16x32_f16 v[70:73], v[118:121], v[134:137], v[70:73]
	v_mfma_f32_16x16x32_f16 v[38:41], v[122:125], v[134:137], v[38:41]
	s_waitcnt lgkmcnt(4)
	v_mfma_f32_16x16x32_f16 v[66:69], v[118:121], v[138:141], v[66:69]
	v_mfma_f32_16x16x32_f16 v[34:37], v[122:125], v[138:141], v[34:37]
	s_waitcnt lgkmcnt(3)
	v_mfma_f32_16x16x32_f16 v[18:21], v[118:121], v[142:145], v[18:21]
	v_mfma_f32_16x16x32_f16 v[2:5], v[122:125], v[142:145], v[2:5]
	s_waitcnt lgkmcnt(2)
	v_mfma_f32_16x16x32_f16 v[26:29], v[118:121], v[146:149], v[26:29]
	v_mfma_f32_16x16x32_f16 v[10:13], v[122:125], v[146:149], v[10:13]
	s_waitcnt lgkmcnt(1)
	v_mfma_f32_16x16x32_f16 v[22:25], v[118:121], v[150:153], v[22:25]
	v_mfma_f32_16x16x32_f16 v[6:9], v[122:125], v[150:153], v[6:9]
	s_waitcnt lgkmcnt(0)
	v_mfma_f32_16x16x32_f16 v[30:33], v[118:121], v[154:157], v[30:33]
	v_mfma_f32_16x16x32_f16 v[14:17], v[122:125], v[154:157], v[14:17]
	s_waitcnt vmcnt(0)
	s_barrier
	ds_read_b128 v[110:113], v158 offset:0
	ds_read_b128 v[114:117], v158 offset:2048
	ds_read_b128 v[118:121], v159 offset:0
	ds_read_b128 v[122:125], v159 offset:2048
	ds_read_b128 v[126:129], v160 offset:16384
	ds_read_b128 v[130:133], v160 offset:18432
	ds_read_b128 v[134:137], v160 offset:20480
	ds_read_b128 v[138:141], v160 offset:22528
	ds_read_b128 v[142:145], v160 offset:24576
	ds_read_b128 v[146:149], v160 offset:26624
	ds_read_b128 v[150:153], v160 offset:28672
	ds_read_b128 v[154:157], v160 offset:30720
	s_waitcnt lgkmcnt(7)
	v_mfma_f32_16x16x32_f16 v[164:167], v[110:113], v[126:129], v[164:167]
	v_mfma_f32_16x16x32_f16 v[62:65], v[114:117], v[126:129], v[62:65]
	ds_read_b128 v[126:129], v160 offset:32768
	s_waitcnt lgkmcnt(7)
	v_mfma_f32_16x16x32_f16 v[86:89], v[110:113], v[130:133], v[86:89]
	v_mfma_f32_16x16x32_f16 v[58:61], v[114:117], v[130:133], v[58:61]
	ds_read_b128 v[130:133], v160 offset:34816
	s_waitcnt lgkmcnt(7)
	v_mfma_f32_16x16x32_f16 v[96:99], v[110:113], v[134:137], v[96:99]
	v_mfma_f32_16x16x32_f16 v[54:57], v[114:117], v[134:137], v[54:57]
	ds_read_b128 v[134:137], v160 offset:36864
	s_waitcnt lgkmcnt(7)
	v_mfma_f32_16x16x32_f16 v[82:85], v[110:113], v[138:141], v[82:85]
	v_mfma_f32_16x16x32_f16 v[50:53], v[114:117], v[138:141], v[50:53]
	ds_read_b128 v[138:141], v160 offset:38912
	s_waitcnt lgkmcnt(7)
	v_mfma_f32_16x16x32_f16 v[78:81], v[110:113], v[142:145], v[78:81]
	v_mfma_f32_16x16x32_f16 v[46:49], v[114:117], v[142:145], v[46:49]
	ds_read_b128 v[142:145], v161 offset:16384
	s_waitcnt lgkmcnt(7)
	v_mfma_f32_16x16x32_f16 v[74:77], v[110:113], v[146:149], v[74:77]
	v_mfma_f32_16x16x32_f16 v[42:45], v[114:117], v[146:149], v[42:45]
	ds_read_b128 v[146:149], v161 offset:18432
	s_waitcnt lgkmcnt(7)
	v_mfma_f32_16x16x32_f16 v[70:73], v[110:113], v[150:153], v[70:73]
	v_mfma_f32_16x16x32_f16 v[38:41], v[114:117], v[150:153], v[38:41]
	ds_read_b128 v[150:153], v161 offset:20480
	s_waitcnt lgkmcnt(7)
	v_mfma_f32_16x16x32_f16 v[66:69], v[110:113], v[154:157], v[66:69]
	v_mfma_f32_16x16x32_f16 v[34:37], v[114:117], v[154:157], v[34:37]
	ds_read_b128 v[154:157], v161 offset:22528
	s_waitcnt lgkmcnt(7)
	v_mfma_f32_16x16x32_f16 v[18:21], v[110:113], v[126:129], v[18:21]
	v_mfma_f32_16x16x32_f16 v[2:5], v[114:117], v[126:129], v[2:5]
	ds_read_b128 v[126:129], v161 offset:24576
	s_waitcnt lgkmcnt(7)
	v_mfma_f32_16x16x32_f16 v[26:29], v[110:113], v[130:133], v[26:29]
	v_mfma_f32_16x16x32_f16 v[10:13], v[114:117], v[130:133], v[10:13]
	ds_read_b128 v[130:133], v161 offset:26624
	s_waitcnt lgkmcnt(7)
	v_mfma_f32_16x16x32_f16 v[22:25], v[110:113], v[134:137], v[22:25]
	v_mfma_f32_16x16x32_f16 v[6:9], v[114:117], v[134:137], v[6:9]
	ds_read_b128 v[134:137], v161 offset:28672
	s_waitcnt lgkmcnt(7)
	v_mfma_f32_16x16x32_f16 v[30:33], v[110:113], v[138:141], v[30:33]
	v_mfma_f32_16x16x32_f16 v[14:17], v[114:117], v[138:141], v[14:17]
	ds_read_b128 v[138:141], v161 offset:30720
	s_waitcnt lgkmcnt(7)
	v_mfma_f32_16x16x32_f16 v[164:167], v[118:121], v[142:145], v[164:167]
	v_mfma_f32_16x16x32_f16 v[62:65], v[122:125], v[142:145], v[62:65]
	ds_read_b128 v[142:145], v161 offset:32768
	s_waitcnt lgkmcnt(7)
	v_mfma_f32_16x16x32_f16 v[86:89], v[118:121], v[146:149], v[86:89]
	v_mfma_f32_16x16x32_f16 v[58:61], v[122:125], v[146:149], v[58:61]
	ds_read_b128 v[146:149], v161 offset:34816
	s_waitcnt lgkmcnt(7)
	v_mfma_f32_16x16x32_f16 v[96:99], v[118:121], v[150:153], v[96:99]
	v_mfma_f32_16x16x32_f16 v[54:57], v[122:125], v[150:153], v[54:57]
	ds_read_b128 v[150:153], v161 offset:36864
	s_waitcnt lgkmcnt(7)
	v_mfma_f32_16x16x32_f16 v[82:85], v[118:121], v[154:157], v[82:85]
	v_mfma_f32_16x16x32_f16 v[50:53], v[122:125], v[154:157], v[50:53]
	ds_read_b128 v[154:157], v161 offset:38912
	s_waitcnt lgkmcnt(0)
	s_barrier
	s_mov_b32 m0, s24
	s_nop 0
	global_load_lds_dwordx4 v100, s[36:37]
	s_mov_b32 m0, s25
	s_nop 0
	global_load_lds_dwordx4 v101, s[36:37]
	s_mov_b32 m0, s26
	s_nop 0
	global_load_lds_dwordx4 v102, s[36:37]
	s_mov_b32 m0, s27
	s_nop 0
	global_load_lds_dwordx4 v103, s[36:37]
	s_mov_b32 m0, s28
	s_nop 0
	global_load_lds_dwordx4 v104, s[38:39]
	s_mov_b32 m0, s29
	s_nop 0
	global_load_lds_dwordx4 v105, s[38:39]
	s_mov_b32 m0, s30
	s_nop 0
	global_load_lds_dwordx4 v106, s[38:39]
	s_mov_b32 m0, s31
	s_nop 0
	global_load_lds_dwordx4 v107, s[38:39]
	s_mov_b32 m0, s32
	s_nop 0
	global_load_lds_dwordx4 v108, s[38:39]
	s_mov_b32 m0, s33
	s_nop 0
	global_load_lds_dwordx4 v109, s[38:39]
	s_add_u32 s36, s36, 0x80
	s_addc_u32 s37, s37, 0
	s_add_u32 s38, s38, 0x80
	s_addc_u32 s39, s39, 0
	s_waitcnt lgkmcnt(7)
	v_mfma_f32_16x16x32_f16 v[78:81], v[118:121], v[126:129], v[78:81]
	v_mfma_f32_16x16x32_f16 v[46:49], v[122:125], v[126:129], v[46:49]
	s_waitcnt lgkmcnt(6)
	v_mfma_f32_16x16x32_f16 v[74:77], v[118:121], v[130:133], v[74:77]
	v_mfma_f32_16x16x32_f16 v[42:45], v[122:125], v[130:133], v[42:45]
	s_waitcnt lgkmcnt(5)
	v_mfma_f32_16x16x32_f16 v[70:73], v[118:121], v[134:137], v[70:73]
	v_mfma_f32_16x16x32_f16 v[38:41], v[122:125], v[134:137], v[38:41]
	s_waitcnt lgkmcnt(4)
	v_mfma_f32_16x16x32_f16 v[66:69], v[118:121], v[138:141], v[66:69]
	v_mfma_f32_16x16x32_f16 v[34:37], v[122:125], v[138:141], v[34:37]
	s_waitcnt lgkmcnt(3)
	v_mfma_f32_16x16x32_f16 v[18:21], v[118:121], v[142:145], v[18:21]
	v_mfma_f32_16x16x32_f16 v[2:5], v[122:125], v[142:145], v[2:5]
	s_waitcnt lgkmcnt(2)
	v_mfma_f32_16x16x32_f16 v[26:29], v[118:121], v[146:149], v[26:29]
	v_mfma_f32_16x16x32_f16 v[10:13], v[122:125], v[146:149], v[10:13]
	s_waitcnt lgkmcnt(1)
	v_mfma_f32_16x16x32_f16 v[22:25], v[118:121], v[150:153], v[22:25]
	v_mfma_f32_16x16x32_f16 v[6:9], v[122:125], v[150:153], v[6:9]
	s_waitcnt lgkmcnt(0)
	v_mfma_f32_16x16x32_f16 v[30:33], v[118:121], v[154:157], v[30:33]
	v_mfma_f32_16x16x32_f16 v[14:17], v[122:125], v[154:157], v[14:17]
	s_waitcnt vmcnt(0)
	s_barrier
	ds_read_b128 v[110:113], v158 offset:0
	ds_read_b128 v[114:117], v158 offset:2048
	ds_read_b128 v[118:121], v159 offset:0
	ds_read_b128 v[122:125], v159 offset:2048
	ds_read_b128 v[126:129], v160 offset:16384
	ds_read_b128 v[130:133], v160 offset:18432
	ds_read_b128 v[134:137], v160 offset:20480
	ds_read_b128 v[138:141], v160 offset:22528
	ds_read_b128 v[142:145], v160 offset:24576
	ds_read_b128 v[146:149], v160 offset:26624
	ds_read_b128 v[150:153], v160 offset:28672
	ds_read_b128 v[154:157], v160 offset:30720
	s_waitcnt lgkmcnt(7)
	v_mfma_f32_16x16x32_f16 v[164:167], v[110:113], v[126:129], v[164:167]
	v_mfma_f32_16x16x32_f16 v[62:65], v[114:117], v[126:129], v[62:65]
	ds_read_b128 v[126:129], v160 offset:32768
	s_waitcnt lgkmcnt(7)
	v_mfma_f32_16x16x32_f16 v[86:89], v[110:113], v[130:133], v[86:89]
	v_mfma_f32_16x16x32_f16 v[58:61], v[114:117], v[130:133], v[58:61]
	ds_read_b128 v[130:133], v160 offset:34816
	s_waitcnt lgkmcnt(7)
	v_mfma_f32_16x16x32_f16 v[96:99], v[110:113], v[134:137], v[96:99]
	v_mfma_f32_16x16x32_f16 v[54:57], v[114:117], v[134:137], v[54:57]
	ds_read_b128 v[134:137], v160 offset:36864
	s_waitcnt lgkmcnt(7)
	v_mfma_f32_16x16x32_f16 v[82:85], v[110:113], v[138:141], v[82:85]
	v_mfma_f32_16x16x32_f16 v[50:53], v[114:117], v[138:141], v[50:53]
	ds_read_b128 v[138:141], v160 offset:38912
	s_waitcnt lgkmcnt(7)
	v_mfma_f32_16x16x32_f16 v[78:81], v[110:113], v[142:145], v[78:81]
	v_mfma_f32_16x16x32_f16 v[46:49], v[114:117], v[142:145], v[46:49]
	ds_read_b128 v[142:145], v161 offset:16384
	s_waitcnt lgkmcnt(7)
	v_mfma_f32_16x16x32_f16 v[74:77], v[110:113], v[146:149], v[74:77]
	v_mfma_f32_16x16x32_f16 v[42:45], v[114:117], v[146:149], v[42:45]
	ds_read_b128 v[146:149], v161 offset:18432
	s_waitcnt lgkmcnt(7)
	v_mfma_f32_16x16x32_f16 v[70:73], v[110:113], v[150:153], v[70:73]
	v_mfma_f32_16x16x32_f16 v[38:41], v[114:117], v[150:153], v[38:41]
	ds_read_b128 v[150:153], v161 offset:20480
	s_waitcnt lgkmcnt(7)
	v_mfma_f32_16x16x32_f16 v[66:69], v[110:113], v[154:157], v[66:69]
	v_mfma_f32_16x16x32_f16 v[34:37], v[114:117], v[154:157], v[34:37]
	ds_read_b128 v[154:157], v161 offset:22528
	s_waitcnt lgkmcnt(7)
	v_mfma_f32_16x16x32_f16 v[18:21], v[110:113], v[126:129], v[18:21]
	v_mfma_f32_16x16x32_f16 v[2:5], v[114:117], v[126:129], v[2:5]
	ds_read_b128 v[126:129], v161 offset:24576
	s_waitcnt lgkmcnt(7)
	v_mfma_f32_16x16x32_f16 v[26:29], v[110:113], v[130:133], v[26:29]
	v_mfma_f32_16x16x32_f16 v[10:13], v[114:117], v[130:133], v[10:13]
	ds_read_b128 v[130:133], v161 offset:26624
	s_waitcnt lgkmcnt(7)
	v_mfma_f32_16x16x32_f16 v[22:25], v[110:113], v[134:137], v[22:25]
	v_mfma_f32_16x16x32_f16 v[6:9], v[114:117], v[134:137], v[6:9]
	ds_read_b128 v[134:137], v161 offset:28672
	s_waitcnt lgkmcnt(7)
	v_mfma_f32_16x16x32_f16 v[30:33], v[110:113], v[138:141], v[30:33]
	v_mfma_f32_16x16x32_f16 v[14:17], v[114:117], v[138:141], v[14:17]
	ds_read_b128 v[138:141], v161 offset:30720
	s_waitcnt lgkmcnt(7)
	v_mfma_f32_16x16x32_f16 v[164:167], v[118:121], v[142:145], v[164:167]
	v_mfma_f32_16x16x32_f16 v[62:65], v[122:125], v[142:145], v[62:65]
	ds_read_b128 v[142:145], v161 offset:32768
	s_waitcnt lgkmcnt(7)
	v_mfma_f32_16x16x32_f16 v[86:89], v[118:121], v[146:149], v[86:89]
	v_mfma_f32_16x16x32_f16 v[58:61], v[122:125], v[146:149], v[58:61]
	ds_read_b128 v[146:149], v161 offset:34816
	s_waitcnt lgkmcnt(7)
	v_mfma_f32_16x16x32_f16 v[96:99], v[118:121], v[150:153], v[96:99]
	v_mfma_f32_16x16x32_f16 v[54:57], v[122:125], v[150:153], v[54:57]
	ds_read_b128 v[150:153], v161 offset:36864
	s_waitcnt lgkmcnt(7)
	v_mfma_f32_16x16x32_f16 v[82:85], v[118:121], v[154:157], v[82:85]
	v_mfma_f32_16x16x32_f16 v[50:53], v[122:125], v[154:157], v[50:53]
	ds_read_b128 v[154:157], v161 offset:38912
	s_waitcnt lgkmcnt(0)
	s_barrier
	s_mov_b32 m0, s24
	s_nop 0
	global_load_lds_dwordx4 v100, s[36:37]
	s_mov_b32 m0, s25
	s_nop 0
	global_load_lds_dwordx4 v101, s[36:37]
	s_mov_b32 m0, s26
	s_nop 0
	global_load_lds_dwordx4 v102, s[36:37]
	s_mov_b32 m0, s27
	s_nop 0
	global_load_lds_dwordx4 v103, s[36:37]
	s_mov_b32 m0, s28
	s_nop 0
	global_load_lds_dwordx4 v104, s[38:39]
	s_mov_b32 m0, s29
	s_nop 0
	global_load_lds_dwordx4 v105, s[38:39]
	s_mov_b32 m0, s30
	s_nop 0
	global_load_lds_dwordx4 v106, s[38:39]
	s_mov_b32 m0, s31
	s_nop 0
	global_load_lds_dwordx4 v107, s[38:39]
	s_mov_b32 m0, s32
	s_nop 0
	global_load_lds_dwordx4 v108, s[38:39]
	s_mov_b32 m0, s33
	s_nop 0
	global_load_lds_dwordx4 v109, s[38:39]
	s_add_u32 s36, s36, 0x80
	s_addc_u32 s37, s37, 0
	s_add_u32 s38, s38, 0x80
	s_addc_u32 s39, s39, 0
	s_waitcnt lgkmcnt(7)
	v_mfma_f32_16x16x32_f16 v[78:81], v[118:121], v[126:129], v[78:81]
	v_mfma_f32_16x16x32_f16 v[46:49], v[122:125], v[126:129], v[46:49]
	s_waitcnt lgkmcnt(6)
	v_mfma_f32_16x16x32_f16 v[74:77], v[118:121], v[130:133], v[74:77]
	v_mfma_f32_16x16x32_f16 v[42:45], v[122:125], v[130:133], v[42:45]
	s_waitcnt lgkmcnt(5)
	v_mfma_f32_16x16x32_f16 v[70:73], v[118:121], v[134:137], v[70:73]
	v_mfma_f32_16x16x32_f16 v[38:41], v[122:125], v[134:137], v[38:41]
	s_waitcnt lgkmcnt(4)
	v_mfma_f32_16x16x32_f16 v[66:69], v[118:121], v[138:141], v[66:69]
	v_mfma_f32_16x16x32_f16 v[34:37], v[122:125], v[138:141], v[34:37]
	s_waitcnt lgkmcnt(3)
	v_mfma_f32_16x16x32_f16 v[18:21], v[118:121], v[142:145], v[18:21]
	v_mfma_f32_16x16x32_f16 v[2:5], v[122:125], v[142:145], v[2:5]
	s_waitcnt lgkmcnt(2)
	v_mfma_f32_16x16x32_f16 v[26:29], v[118:121], v[146:149], v[26:29]
	v_mfma_f32_16x16x32_f16 v[10:13], v[122:125], v[146:149], v[10:13]
	s_waitcnt lgkmcnt(1)
	v_mfma_f32_16x16x32_f16 v[22:25], v[118:121], v[150:153], v[22:25]
	v_mfma_f32_16x16x32_f16 v[6:9], v[122:125], v[150:153], v[6:9]
	s_waitcnt lgkmcnt(0)
	v_mfma_f32_16x16x32_f16 v[30:33], v[118:121], v[154:157], v[30:33]
	v_mfma_f32_16x16x32_f16 v[14:17], v[122:125], v[154:157], v[14:17]
	s_waitcnt vmcnt(0)
	s_barrier
	ds_read_b128 v[110:113], v158 offset:0
	ds_read_b128 v[114:117], v158 offset:2048
	ds_read_b128 v[118:121], v159 offset:0
	ds_read_b128 v[122:125], v159 offset:2048
	ds_read_b128 v[126:129], v160 offset:16384
	ds_read_b128 v[130:133], v160 offset:18432
	ds_read_b128 v[134:137], v160 offset:20480
	ds_read_b128 v[138:141], v160 offset:22528
	ds_read_b128 v[142:145], v160 offset:24576
	ds_read_b128 v[146:149], v160 offset:26624
	ds_read_b128 v[150:153], v160 offset:28672
	ds_read_b128 v[154:157], v160 offset:30720
	s_waitcnt lgkmcnt(7)
	v_mfma_f32_16x16x32_f16 v[164:167], v[110:113], v[126:129], v[164:167]
	v_mfma_f32_16x16x32_f16 v[62:65], v[114:117], v[126:129], v[62:65]
	ds_read_b128 v[126:129], v160 offset:32768
	s_waitcnt lgkmcnt(7)
	v_mfma_f32_16x16x32_f16 v[86:89], v[110:113], v[130:133], v[86:89]
	v_mfma_f32_16x16x32_f16 v[58:61], v[114:117], v[130:133], v[58:61]
	ds_read_b128 v[130:133], v160 offset:34816
	s_waitcnt lgkmcnt(7)
	v_mfma_f32_16x16x32_f16 v[96:99], v[110:113], v[134:137], v[96:99]
	v_mfma_f32_16x16x32_f16 v[54:57], v[114:117], v[134:137], v[54:57]
	ds_read_b128 v[134:137], v160 offset:36864
	s_waitcnt lgkmcnt(7)
	v_mfma_f32_16x16x32_f16 v[82:85], v[110:113], v[138:141], v[82:85]
	v_mfma_f32_16x16x32_f16 v[50:53], v[114:117], v[138:141], v[50:53]
	ds_read_b128 v[138:141], v160 offset:38912
	s_waitcnt lgkmcnt(7)
	v_mfma_f32_16x16x32_f16 v[78:81], v[110:113], v[142:145], v[78:81]
	v_mfma_f32_16x16x32_f16 v[46:49], v[114:117], v[142:145], v[46:49]
	ds_read_b128 v[142:145], v161 offset:16384
	s_waitcnt lgkmcnt(7)
	v_mfma_f32_16x16x32_f16 v[74:77], v[110:113], v[146:149], v[74:77]
	v_mfma_f32_16x16x32_f16 v[42:45], v[114:117], v[146:149], v[42:45]
	ds_read_b128 v[146:149], v161 offset:18432
	s_waitcnt lgkmcnt(7)
	v_mfma_f32_16x16x32_f16 v[70:73], v[110:113], v[150:153], v[70:73]
	v_mfma_f32_16x16x32_f16 v[38:41], v[114:117], v[150:153], v[38:41]
	ds_read_b128 v[150:153], v161 offset:20480
	s_waitcnt lgkmcnt(7)
	v_mfma_f32_16x16x32_f16 v[66:69], v[110:113], v[154:157], v[66:69]
	v_mfma_f32_16x16x32_f16 v[34:37], v[114:117], v[154:157], v[34:37]
	ds_read_b128 v[154:157], v161 offset:22528
	s_waitcnt lgkmcnt(7)
	v_mfma_f32_16x16x32_f16 v[18:21], v[110:113], v[126:129], v[18:21]
	v_mfma_f32_16x16x32_f16 v[2:5], v[114:117], v[126:129], v[2:5]
	ds_read_b128 v[126:129], v161 offset:24576
	s_waitcnt lgkmcnt(7)
	v_mfma_f32_16x16x32_f16 v[26:29], v[110:113], v[130:133], v[26:29]
	v_mfma_f32_16x16x32_f16 v[10:13], v[114:117], v[130:133], v[10:13]
	ds_read_b128 v[130:133], v161 offset:26624
	s_waitcnt lgkmcnt(7)
	v_mfma_f32_16x16x32_f16 v[22:25], v[110:113], v[134:137], v[22:25]
	v_mfma_f32_16x16x32_f16 v[6:9], v[114:117], v[134:137], v[6:9]
	ds_read_b128 v[134:137], v161 offset:28672
	s_waitcnt lgkmcnt(7)
	v_mfma_f32_16x16x32_f16 v[30:33], v[110:113], v[138:141], v[30:33]
	v_mfma_f32_16x16x32_f16 v[14:17], v[114:117], v[138:141], v[14:17]
	ds_read_b128 v[138:141], v161 offset:30720
	s_waitcnt lgkmcnt(7)
	v_mfma_f32_16x16x32_f16 v[164:167], v[118:121], v[142:145], v[164:167]
	v_mfma_f32_16x16x32_f16 v[62:65], v[122:125], v[142:145], v[62:65]
	ds_read_b128 v[142:145], v161 offset:32768
	s_waitcnt lgkmcnt(7)
	v_mfma_f32_16x16x32_f16 v[86:89], v[118:121], v[146:149], v[86:89]
	v_mfma_f32_16x16x32_f16 v[58:61], v[122:125], v[146:149], v[58:61]
	ds_read_b128 v[146:149], v161 offset:34816
	s_waitcnt lgkmcnt(7)
	v_mfma_f32_16x16x32_f16 v[96:99], v[118:121], v[150:153], v[96:99]
	v_mfma_f32_16x16x32_f16 v[54:57], v[122:125], v[150:153], v[54:57]
	ds_read_b128 v[150:153], v161 offset:36864
	s_waitcnt lgkmcnt(7)
	v_mfma_f32_16x16x32_f16 v[82:85], v[118:121], v[154:157], v[82:85]
	v_mfma_f32_16x16x32_f16 v[50:53], v[122:125], v[154:157], v[50:53]
	ds_read_b128 v[154:157], v161 offset:38912
	s_waitcnt lgkmcnt(0)
	s_barrier
	s_mov_b32 m0, s24
	s_nop 0
	global_load_lds_dwordx4 v100, s[36:37]
	s_mov_b32 m0, s25
	s_nop 0
	global_load_lds_dwordx4 v101, s[36:37]
	s_mov_b32 m0, s26
	s_nop 0
	global_load_lds_dwordx4 v102, s[36:37]
	s_mov_b32 m0, s27
	s_nop 0
	global_load_lds_dwordx4 v103, s[36:37]
	s_mov_b32 m0, s28
	s_nop 0
	global_load_lds_dwordx4 v104, s[38:39]
	s_mov_b32 m0, s29
	s_nop 0
	global_load_lds_dwordx4 v105, s[38:39]
	s_mov_b32 m0, s30
	s_nop 0
	global_load_lds_dwordx4 v106, s[38:39]
	s_mov_b32 m0, s31
	s_nop 0
	global_load_lds_dwordx4 v107, s[38:39]
	s_mov_b32 m0, s32
	s_nop 0
	global_load_lds_dwordx4 v108, s[38:39]
	s_mov_b32 m0, s33
	s_nop 0
	global_load_lds_dwordx4 v109, s[38:39]
	s_add_u32 s36, s36, 0x80
	s_addc_u32 s37, s37, 0
	s_add_u32 s38, s38, 0x80
	s_addc_u32 s39, s39, 0
	s_waitcnt lgkmcnt(7)
	v_mfma_f32_16x16x32_f16 v[78:81], v[118:121], v[126:129], v[78:81]
	v_mfma_f32_16x16x32_f16 v[46:49], v[122:125], v[126:129], v[46:49]
	s_waitcnt lgkmcnt(6)
	v_mfma_f32_16x16x32_f16 v[74:77], v[118:121], v[130:133], v[74:77]
	v_mfma_f32_16x16x32_f16 v[42:45], v[122:125], v[130:133], v[42:45]
	s_waitcnt lgkmcnt(5)
	v_mfma_f32_16x16x32_f16 v[70:73], v[118:121], v[134:137], v[70:73]
	v_mfma_f32_16x16x32_f16 v[38:41], v[122:125], v[134:137], v[38:41]
	s_waitcnt lgkmcnt(4)
	v_mfma_f32_16x16x32_f16 v[66:69], v[118:121], v[138:141], v[66:69]
	v_mfma_f32_16x16x32_f16 v[34:37], v[122:125], v[138:141], v[34:37]
	s_waitcnt lgkmcnt(3)
	v_mfma_f32_16x16x32_f16 v[18:21], v[118:121], v[142:145], v[18:21]
	v_mfma_f32_16x16x32_f16 v[2:5], v[122:125], v[142:145], v[2:5]
	s_waitcnt lgkmcnt(2)
	v_mfma_f32_16x16x32_f16 v[26:29], v[118:121], v[146:149], v[26:29]
	v_mfma_f32_16x16x32_f16 v[10:13], v[122:125], v[146:149], v[10:13]
	s_waitcnt lgkmcnt(1)
	v_mfma_f32_16x16x32_f16 v[22:25], v[118:121], v[150:153], v[22:25]
	v_mfma_f32_16x16x32_f16 v[6:9], v[122:125], v[150:153], v[6:9]
	s_waitcnt lgkmcnt(0)
	v_mfma_f32_16x16x32_f16 v[30:33], v[118:121], v[154:157], v[30:33]
	v_mfma_f32_16x16x32_f16 v[14:17], v[122:125], v[154:157], v[14:17]
	s_waitcnt vmcnt(0)
	s_barrier
	ds_read_b128 v[110:113], v158 offset:0
	ds_read_b128 v[114:117], v158 offset:2048
	ds_read_b128 v[118:121], v159 offset:0
	ds_read_b128 v[122:125], v159 offset:2048
	ds_read_b128 v[126:129], v160 offset:16384
	ds_read_b128 v[130:133], v160 offset:18432
	ds_read_b128 v[134:137], v160 offset:20480
	ds_read_b128 v[138:141], v160 offset:22528
	ds_read_b128 v[142:145], v160 offset:24576
	ds_read_b128 v[146:149], v160 offset:26624
	ds_read_b128 v[150:153], v160 offset:28672
	ds_read_b128 v[154:157], v160 offset:30720
	s_waitcnt lgkmcnt(7)
	v_mfma_f32_16x16x32_f16 v[164:167], v[110:113], v[126:129], v[164:167]
	v_mfma_f32_16x16x32_f16 v[62:65], v[114:117], v[126:129], v[62:65]
	ds_read_b128 v[126:129], v160 offset:32768
	s_waitcnt lgkmcnt(7)
	v_mfma_f32_16x16x32_f16 v[86:89], v[110:113], v[130:133], v[86:89]
	v_mfma_f32_16x16x32_f16 v[58:61], v[114:117], v[130:133], v[58:61]
	ds_read_b128 v[130:133], v160 offset:34816
	s_waitcnt lgkmcnt(7)
	v_mfma_f32_16x16x32_f16 v[96:99], v[110:113], v[134:137], v[96:99]
	v_mfma_f32_16x16x32_f16 v[54:57], v[114:117], v[134:137], v[54:57]
	ds_read_b128 v[134:137], v160 offset:36864
	s_waitcnt lgkmcnt(7)
	v_mfma_f32_16x16x32_f16 v[82:85], v[110:113], v[138:141], v[82:85]
	v_mfma_f32_16x16x32_f16 v[50:53], v[114:117], v[138:141], v[50:53]
	ds_read_b128 v[138:141], v160 offset:38912
	s_waitcnt lgkmcnt(7)
	v_mfma_f32_16x16x32_f16 v[78:81], v[110:113], v[142:145], v[78:81]
	v_mfma_f32_16x16x32_f16 v[46:49], v[114:117], v[142:145], v[46:49]
	ds_read_b128 v[142:145], v161 offset:16384
	s_waitcnt lgkmcnt(7)
	v_mfma_f32_16x16x32_f16 v[74:77], v[110:113], v[146:149], v[74:77]
	v_mfma_f32_16x16x32_f16 v[42:45], v[114:117], v[146:149], v[42:45]
	ds_read_b128 v[146:149], v161 offset:18432
	s_waitcnt lgkmcnt(7)
	v_mfma_f32_16x16x32_f16 v[70:73], v[110:113], v[150:153], v[70:73]
	v_mfma_f32_16x16x32_f16 v[38:41], v[114:117], v[150:153], v[38:41]
	ds_read_b128 v[150:153], v161 offset:20480
	s_waitcnt lgkmcnt(7)
	v_mfma_f32_16x16x32_f16 v[66:69], v[110:113], v[154:157], v[66:69]
	v_mfma_f32_16x16x32_f16 v[34:37], v[114:117], v[154:157], v[34:37]
	ds_read_b128 v[154:157], v161 offset:22528
	s_waitcnt lgkmcnt(7)
	v_mfma_f32_16x16x32_f16 v[18:21], v[110:113], v[126:129], v[18:21]
	v_mfma_f32_16x16x32_f16 v[2:5], v[114:117], v[126:129], v[2:5]
	ds_read_b128 v[126:129], v161 offset:24576
	s_waitcnt lgkmcnt(7)
	v_mfma_f32_16x16x32_f16 v[26:29], v[110:113], v[130:133], v[26:29]
	v_mfma_f32_16x16x32_f16 v[10:13], v[114:117], v[130:133], v[10:13]
	ds_read_b128 v[130:133], v161 offset:26624
	s_waitcnt lgkmcnt(7)
	v_mfma_f32_16x16x32_f16 v[22:25], v[110:113], v[134:137], v[22:25]
	v_mfma_f32_16x16x32_f16 v[6:9], v[114:117], v[134:137], v[6:9]
	ds_read_b128 v[134:137], v161 offset:28672
	s_waitcnt lgkmcnt(7)
	v_mfma_f32_16x16x32_f16 v[30:33], v[110:113], v[138:141], v[30:33]
	v_mfma_f32_16x16x32_f16 v[14:17], v[114:117], v[138:141], v[14:17]
	ds_read_b128 v[138:141], v161 offset:30720
	s_waitcnt lgkmcnt(7)
	v_mfma_f32_16x16x32_f16 v[164:167], v[118:121], v[142:145], v[164:167]
	v_mfma_f32_16x16x32_f16 v[62:65], v[122:125], v[142:145], v[62:65]
	ds_read_b128 v[142:145], v161 offset:32768
	s_waitcnt lgkmcnt(7)
	v_mfma_f32_16x16x32_f16 v[86:89], v[118:121], v[146:149], v[86:89]
	v_mfma_f32_16x16x32_f16 v[58:61], v[122:125], v[146:149], v[58:61]
	ds_read_b128 v[146:149], v161 offset:34816
	s_waitcnt lgkmcnt(7)
	v_mfma_f32_16x16x32_f16 v[96:99], v[118:121], v[150:153], v[96:99]
	v_mfma_f32_16x16x32_f16 v[54:57], v[122:125], v[150:153], v[54:57]
	ds_read_b128 v[150:153], v161 offset:36864
	s_waitcnt lgkmcnt(7)
	v_mfma_f32_16x16x32_f16 v[82:85], v[118:121], v[154:157], v[82:85]
	v_mfma_f32_16x16x32_f16 v[50:53], v[122:125], v[154:157], v[50:53]
	ds_read_b128 v[154:157], v161 offset:38912
	s_waitcnt lgkmcnt(0)
	s_barrier
	s_mov_b32 m0, s24
	s_nop 0
	global_load_lds_dwordx4 v100, s[36:37]
	s_mov_b32 m0, s25
	s_nop 0
	global_load_lds_dwordx4 v101, s[36:37]
	s_mov_b32 m0, s26
	s_nop 0
	global_load_lds_dwordx4 v102, s[36:37]
	s_mov_b32 m0, s27
	s_nop 0
	global_load_lds_dwordx4 v103, s[36:37]
	s_mov_b32 m0, s28
	s_nop 0
	global_load_lds_dwordx4 v104, s[38:39]
	s_mov_b32 m0, s29
	s_nop 0
	global_load_lds_dwordx4 v105, s[38:39]
	s_mov_b32 m0, s30
	s_nop 0
	global_load_lds_dwordx4 v106, s[38:39]
	s_mov_b32 m0, s31
	s_nop 0
	global_load_lds_dwordx4 v107, s[38:39]
	s_mov_b32 m0, s32
	s_nop 0
	global_load_lds_dwordx4 v108, s[38:39]
	s_mov_b32 m0, s33
	s_nop 0
	global_load_lds_dwordx4 v109, s[38:39]
	s_add_u32 s36, s36, 0x80
	s_addc_u32 s37, s37, 0
	s_add_u32 s38, s38, 0x80
	s_addc_u32 s39, s39, 0
	s_waitcnt lgkmcnt(7)
	v_mfma_f32_16x16x32_f16 v[78:81], v[118:121], v[126:129], v[78:81]
	v_mfma_f32_16x16x32_f16 v[46:49], v[122:125], v[126:129], v[46:49]
	s_waitcnt lgkmcnt(6)
	v_mfma_f32_16x16x32_f16 v[74:77], v[118:121], v[130:133], v[74:77]
	v_mfma_f32_16x16x32_f16 v[42:45], v[122:125], v[130:133], v[42:45]
	s_waitcnt lgkmcnt(5)
	v_mfma_f32_16x16x32_f16 v[70:73], v[118:121], v[134:137], v[70:73]
	v_mfma_f32_16x16x32_f16 v[38:41], v[122:125], v[134:137], v[38:41]
	s_waitcnt lgkmcnt(4)
	v_mfma_f32_16x16x32_f16 v[66:69], v[118:121], v[138:141], v[66:69]
	v_mfma_f32_16x16x32_f16 v[34:37], v[122:125], v[138:141], v[34:37]
	s_waitcnt lgkmcnt(3)
	v_mfma_f32_16x16x32_f16 v[18:21], v[118:121], v[142:145], v[18:21]
	v_mfma_f32_16x16x32_f16 v[2:5], v[122:125], v[142:145], v[2:5]
	s_waitcnt lgkmcnt(2)
	v_mfma_f32_16x16x32_f16 v[26:29], v[118:121], v[146:149], v[26:29]
	v_mfma_f32_16x16x32_f16 v[10:13], v[122:125], v[146:149], v[10:13]
	s_waitcnt lgkmcnt(1)
	v_mfma_f32_16x16x32_f16 v[22:25], v[118:121], v[150:153], v[22:25]
	v_mfma_f32_16x16x32_f16 v[6:9], v[122:125], v[150:153], v[6:9]
	s_waitcnt lgkmcnt(0)
	v_mfma_f32_16x16x32_f16 v[30:33], v[118:121], v[154:157], v[30:33]
	v_mfma_f32_16x16x32_f16 v[14:17], v[122:125], v[154:157], v[14:17]
	s_waitcnt vmcnt(0)
	s_barrier
	ds_read_b128 v[110:113], v158 offset:0
	ds_read_b128 v[114:117], v158 offset:2048
	ds_read_b128 v[118:121], v159 offset:0
	ds_read_b128 v[122:125], v159 offset:2048
	ds_read_b128 v[126:129], v160 offset:16384
	ds_read_b128 v[130:133], v160 offset:18432
	ds_read_b128 v[134:137], v160 offset:20480
	ds_read_b128 v[138:141], v160 offset:22528
	ds_read_b128 v[142:145], v160 offset:24576
	ds_read_b128 v[146:149], v160 offset:26624
	ds_read_b128 v[150:153], v160 offset:28672
	ds_read_b128 v[154:157], v160 offset:30720
	s_waitcnt lgkmcnt(7)
	v_mfma_f32_16x16x32_f16 v[164:167], v[110:113], v[126:129], v[164:167]
	v_mfma_f32_16x16x32_f16 v[62:65], v[114:117], v[126:129], v[62:65]
	ds_read_b128 v[126:129], v160 offset:32768
	s_waitcnt lgkmcnt(7)
	v_mfma_f32_16x16x32_f16 v[86:89], v[110:113], v[130:133], v[86:89]
	v_mfma_f32_16x16x32_f16 v[58:61], v[114:117], v[130:133], v[58:61]
	ds_read_b128 v[130:133], v160 offset:34816
	s_waitcnt lgkmcnt(7)
	v_mfma_f32_16x16x32_f16 v[96:99], v[110:113], v[134:137], v[96:99]
	v_mfma_f32_16x16x32_f16 v[54:57], v[114:117], v[134:137], v[54:57]
	ds_read_b128 v[134:137], v160 offset:36864
	s_waitcnt lgkmcnt(7)
	v_mfma_f32_16x16x32_f16 v[82:85], v[110:113], v[138:141], v[82:85]
	v_mfma_f32_16x16x32_f16 v[50:53], v[114:117], v[138:141], v[50:53]
	ds_read_b128 v[138:141], v160 offset:38912
	s_waitcnt lgkmcnt(7)
	v_mfma_f32_16x16x32_f16 v[78:81], v[110:113], v[142:145], v[78:81]
	v_mfma_f32_16x16x32_f16 v[46:49], v[114:117], v[142:145], v[46:49]
	ds_read_b128 v[142:145], v161 offset:16384
	s_waitcnt lgkmcnt(7)
	v_mfma_f32_16x16x32_f16 v[74:77], v[110:113], v[146:149], v[74:77]
	v_mfma_f32_16x16x32_f16 v[42:45], v[114:117], v[146:149], v[42:45]
	ds_read_b128 v[146:149], v161 offset:18432
	s_waitcnt lgkmcnt(7)
	v_mfma_f32_16x16x32_f16 v[70:73], v[110:113], v[150:153], v[70:73]
	v_mfma_f32_16x16x32_f16 v[38:41], v[114:117], v[150:153], v[38:41]
	ds_read_b128 v[150:153], v161 offset:20480
	s_waitcnt lgkmcnt(7)
	v_mfma_f32_16x16x32_f16 v[66:69], v[110:113], v[154:157], v[66:69]
	v_mfma_f32_16x16x32_f16 v[34:37], v[114:117], v[154:157], v[34:37]
	ds_read_b128 v[154:157], v161 offset:22528
	s_waitcnt lgkmcnt(7)
	v_mfma_f32_16x16x32_f16 v[18:21], v[110:113], v[126:129], v[18:21]
	v_mfma_f32_16x16x32_f16 v[2:5], v[114:117], v[126:129], v[2:5]
	ds_read_b128 v[126:129], v161 offset:24576
	s_waitcnt lgkmcnt(7)
	v_mfma_f32_16x16x32_f16 v[26:29], v[110:113], v[130:133], v[26:29]
	v_mfma_f32_16x16x32_f16 v[10:13], v[114:117], v[130:133], v[10:13]
	ds_read_b128 v[130:133], v161 offset:26624
	s_waitcnt lgkmcnt(7)
	v_mfma_f32_16x16x32_f16 v[22:25], v[110:113], v[134:137], v[22:25]
	v_mfma_f32_16x16x32_f16 v[6:9], v[114:117], v[134:137], v[6:9]
	ds_read_b128 v[134:137], v161 offset:28672
	s_waitcnt lgkmcnt(7)
	v_mfma_f32_16x16x32_f16 v[30:33], v[110:113], v[138:141], v[30:33]
	v_mfma_f32_16x16x32_f16 v[14:17], v[114:117], v[138:141], v[14:17]
	ds_read_b128 v[138:141], v161 offset:30720
	s_waitcnt lgkmcnt(7)
	v_mfma_f32_16x16x32_f16 v[164:167], v[118:121], v[142:145], v[164:167]
	v_mfma_f32_16x16x32_f16 v[62:65], v[122:125], v[142:145], v[62:65]
	ds_read_b128 v[142:145], v161 offset:32768
	s_waitcnt lgkmcnt(7)
	v_mfma_f32_16x16x32_f16 v[86:89], v[118:121], v[146:149], v[86:89]
	v_mfma_f32_16x16x32_f16 v[58:61], v[122:125], v[146:149], v[58:61]
	ds_read_b128 v[146:149], v161 offset:34816
	s_waitcnt lgkmcnt(7)
	v_mfma_f32_16x16x32_f16 v[96:99], v[118:121], v[150:153], v[96:99]
	v_mfma_f32_16x16x32_f16 v[54:57], v[122:125], v[150:153], v[54:57]
	ds_read_b128 v[150:153], v161 offset:36864
	s_waitcnt lgkmcnt(7)
	v_mfma_f32_16x16x32_f16 v[82:85], v[118:121], v[154:157], v[82:85]
	v_mfma_f32_16x16x32_f16 v[50:53], v[122:125], v[154:157], v[50:53]
	ds_read_b128 v[154:157], v161 offset:38912
	s_waitcnt lgkmcnt(0)
	s_barrier
	s_mov_b32 m0, s24
	s_nop 0
	global_load_lds_dwordx4 v100, s[36:37]
	s_mov_b32 m0, s25
	s_nop 0
	global_load_lds_dwordx4 v101, s[36:37]
	s_mov_b32 m0, s26
	s_nop 0
	global_load_lds_dwordx4 v102, s[36:37]
	s_mov_b32 m0, s27
	s_nop 0
	global_load_lds_dwordx4 v103, s[36:37]
	s_mov_b32 m0, s28
	s_nop 0
	global_load_lds_dwordx4 v104, s[38:39]
	s_mov_b32 m0, s29
	s_nop 0
	global_load_lds_dwordx4 v105, s[38:39]
	s_mov_b32 m0, s30
	s_nop 0
	global_load_lds_dwordx4 v106, s[38:39]
	s_mov_b32 m0, s31
	s_nop 0
	global_load_lds_dwordx4 v107, s[38:39]
	s_mov_b32 m0, s32
	s_nop 0
	global_load_lds_dwordx4 v108, s[38:39]
	s_mov_b32 m0, s33
	s_nop 0
	global_load_lds_dwordx4 v109, s[38:39]
	s_add_u32 s36, s36, 0x80
	s_addc_u32 s37, s37, 0
	s_add_u32 s38, s38, 0x80
	s_addc_u32 s39, s39, 0
	s_waitcnt lgkmcnt(7)
	v_mfma_f32_16x16x32_f16 v[78:81], v[118:121], v[126:129], v[78:81]
	v_mfma_f32_16x16x32_f16 v[46:49], v[122:125], v[126:129], v[46:49]
	s_waitcnt lgkmcnt(6)
	v_mfma_f32_16x16x32_f16 v[74:77], v[118:121], v[130:133], v[74:77]
	v_mfma_f32_16x16x32_f16 v[42:45], v[122:125], v[130:133], v[42:45]
	s_waitcnt lgkmcnt(5)
	v_mfma_f32_16x16x32_f16 v[70:73], v[118:121], v[134:137], v[70:73]
	v_mfma_f32_16x16x32_f16 v[38:41], v[122:125], v[134:137], v[38:41]
	s_waitcnt lgkmcnt(4)
	v_mfma_f32_16x16x32_f16 v[66:69], v[118:121], v[138:141], v[66:69]
	v_mfma_f32_16x16x32_f16 v[34:37], v[122:125], v[138:141], v[34:37]
	s_waitcnt lgkmcnt(3)
	v_mfma_f32_16x16x32_f16 v[18:21], v[118:121], v[142:145], v[18:21]
	v_mfma_f32_16x16x32_f16 v[2:5], v[122:125], v[142:145], v[2:5]
	s_waitcnt lgkmcnt(2)
	v_mfma_f32_16x16x32_f16 v[26:29], v[118:121], v[146:149], v[26:29]
	v_mfma_f32_16x16x32_f16 v[10:13], v[122:125], v[146:149], v[10:13]
	s_waitcnt lgkmcnt(1)
	v_mfma_f32_16x16x32_f16 v[22:25], v[118:121], v[150:153], v[22:25]
	v_mfma_f32_16x16x32_f16 v[6:9], v[122:125], v[150:153], v[6:9]
	s_waitcnt lgkmcnt(0)
	v_mfma_f32_16x16x32_f16 v[30:33], v[118:121], v[154:157], v[30:33]
	v_mfma_f32_16x16x32_f16 v[14:17], v[122:125], v[154:157], v[14:17]
	s_waitcnt vmcnt(0)
	s_barrier
	ds_read_b128 v[110:113], v158 offset:0
	ds_read_b128 v[114:117], v158 offset:2048
	ds_read_b128 v[118:121], v159 offset:0
	ds_read_b128 v[122:125], v159 offset:2048
	ds_read_b128 v[126:129], v160 offset:16384
	ds_read_b128 v[130:133], v160 offset:18432
	ds_read_b128 v[134:137], v160 offset:20480
	ds_read_b128 v[138:141], v160 offset:22528
	ds_read_b128 v[142:145], v160 offset:24576
	ds_read_b128 v[146:149], v160 offset:26624
	ds_read_b128 v[150:153], v160 offset:28672
	ds_read_b128 v[154:157], v160 offset:30720
	s_waitcnt lgkmcnt(7)
	v_mfma_f32_16x16x32_f16 v[164:167], v[110:113], v[126:129], v[164:167]
	v_mfma_f32_16x16x32_f16 v[62:65], v[114:117], v[126:129], v[62:65]
	ds_read_b128 v[126:129], v160 offset:32768
	s_waitcnt lgkmcnt(7)
	v_mfma_f32_16x16x32_f16 v[86:89], v[110:113], v[130:133], v[86:89]
	v_mfma_f32_16x16x32_f16 v[58:61], v[114:117], v[130:133], v[58:61]
	ds_read_b128 v[130:133], v160 offset:34816
	s_waitcnt lgkmcnt(7)
	v_mfma_f32_16x16x32_f16 v[96:99], v[110:113], v[134:137], v[96:99]
	v_mfma_f32_16x16x32_f16 v[54:57], v[114:117], v[134:137], v[54:57]
	ds_read_b128 v[134:137], v160 offset:36864
	s_waitcnt lgkmcnt(7)
	v_mfma_f32_16x16x32_f16 v[82:85], v[110:113], v[138:141], v[82:85]
	v_mfma_f32_16x16x32_f16 v[50:53], v[114:117], v[138:141], v[50:53]
	ds_read_b128 v[138:141], v160 offset:38912
	s_waitcnt lgkmcnt(7)
	v_mfma_f32_16x16x32_f16 v[78:81], v[110:113], v[142:145], v[78:81]
	v_mfma_f32_16x16x32_f16 v[46:49], v[114:117], v[142:145], v[46:49]
	ds_read_b128 v[142:145], v161 offset:16384
	s_waitcnt lgkmcnt(7)
	v_mfma_f32_16x16x32_f16 v[74:77], v[110:113], v[146:149], v[74:77]
	v_mfma_f32_16x16x32_f16 v[42:45], v[114:117], v[146:149], v[42:45]
	ds_read_b128 v[146:149], v161 offset:18432
	s_waitcnt lgkmcnt(7)
	v_mfma_f32_16x16x32_f16 v[70:73], v[110:113], v[150:153], v[70:73]
	v_mfma_f32_16x16x32_f16 v[38:41], v[114:117], v[150:153], v[38:41]
	ds_read_b128 v[150:153], v161 offset:20480
	s_waitcnt lgkmcnt(7)
	v_mfma_f32_16x16x32_f16 v[66:69], v[110:113], v[154:157], v[66:69]
	v_mfma_f32_16x16x32_f16 v[34:37], v[114:117], v[154:157], v[34:37]
	ds_read_b128 v[154:157], v161 offset:22528
	s_waitcnt lgkmcnt(7)
	v_mfma_f32_16x16x32_f16 v[18:21], v[110:113], v[126:129], v[18:21]
	v_mfma_f32_16x16x32_f16 v[2:5], v[114:117], v[126:129], v[2:5]
	ds_read_b128 v[126:129], v161 offset:24576
	s_waitcnt lgkmcnt(7)
	v_mfma_f32_16x16x32_f16 v[26:29], v[110:113], v[130:133], v[26:29]
	v_mfma_f32_16x16x32_f16 v[10:13], v[114:117], v[130:133], v[10:13]
	ds_read_b128 v[130:133], v161 offset:26624
	s_waitcnt lgkmcnt(7)
	v_mfma_f32_16x16x32_f16 v[22:25], v[110:113], v[134:137], v[22:25]
	v_mfma_f32_16x16x32_f16 v[6:9], v[114:117], v[134:137], v[6:9]
	ds_read_b128 v[134:137], v161 offset:28672
	s_waitcnt lgkmcnt(7)
	v_mfma_f32_16x16x32_f16 v[30:33], v[110:113], v[138:141], v[30:33]
	v_mfma_f32_16x16x32_f16 v[14:17], v[114:117], v[138:141], v[14:17]
	ds_read_b128 v[138:141], v161 offset:30720
	s_waitcnt lgkmcnt(7)
	v_mfma_f32_16x16x32_f16 v[164:167], v[118:121], v[142:145], v[164:167]
	v_mfma_f32_16x16x32_f16 v[62:65], v[122:125], v[142:145], v[62:65]
	ds_read_b128 v[142:145], v161 offset:32768
	s_waitcnt lgkmcnt(7)
	v_mfma_f32_16x16x32_f16 v[86:89], v[118:121], v[146:149], v[86:89]
	v_mfma_f32_16x16x32_f16 v[58:61], v[122:125], v[146:149], v[58:61]
	ds_read_b128 v[146:149], v161 offset:34816
	s_waitcnt lgkmcnt(7)
	v_mfma_f32_16x16x32_f16 v[96:99], v[118:121], v[150:153], v[96:99]
	v_mfma_f32_16x16x32_f16 v[54:57], v[122:125], v[150:153], v[54:57]
	ds_read_b128 v[150:153], v161 offset:36864
	s_waitcnt lgkmcnt(7)
	v_mfma_f32_16x16x32_f16 v[82:85], v[118:121], v[154:157], v[82:85]
	v_mfma_f32_16x16x32_f16 v[50:53], v[122:125], v[154:157], v[50:53]
	ds_read_b128 v[154:157], v161 offset:38912
	s_waitcnt lgkmcnt(0)
	s_barrier
	s_mov_b32 m0, s24
	s_nop 0
	global_load_lds_dwordx4 v100, s[36:37]
	s_mov_b32 m0, s25
	s_nop 0
	global_load_lds_dwordx4 v101, s[36:37]
	s_mov_b32 m0, s26
	s_nop 0
	global_load_lds_dwordx4 v102, s[36:37]
	s_mov_b32 m0, s27
	s_nop 0
	global_load_lds_dwordx4 v103, s[36:37]
	s_mov_b32 m0, s28
	s_nop 0
	global_load_lds_dwordx4 v104, s[38:39]
	s_mov_b32 m0, s29
	s_nop 0
	global_load_lds_dwordx4 v105, s[38:39]
	s_mov_b32 m0, s30
	s_nop 0
	global_load_lds_dwordx4 v106, s[38:39]
	s_mov_b32 m0, s31
	s_nop 0
	global_load_lds_dwordx4 v107, s[38:39]
	s_mov_b32 m0, s32
	s_nop 0
	global_load_lds_dwordx4 v108, s[38:39]
	s_mov_b32 m0, s33
	s_nop 0
	global_load_lds_dwordx4 v109, s[38:39]
	s_add_u32 s36, s36, 0x80
	s_addc_u32 s37, s37, 0
	s_add_u32 s38, s38, 0x80
	s_addc_u32 s39, s39, 0
	s_waitcnt lgkmcnt(7)
	v_mfma_f32_16x16x32_f16 v[78:81], v[118:121], v[126:129], v[78:81]
	v_mfma_f32_16x16x32_f16 v[46:49], v[122:125], v[126:129], v[46:49]
	s_waitcnt lgkmcnt(6)
	v_mfma_f32_16x16x32_f16 v[74:77], v[118:121], v[130:133], v[74:77]
	v_mfma_f32_16x16x32_f16 v[42:45], v[122:125], v[130:133], v[42:45]
	s_waitcnt lgkmcnt(5)
	v_mfma_f32_16x16x32_f16 v[70:73], v[118:121], v[134:137], v[70:73]
	v_mfma_f32_16x16x32_f16 v[38:41], v[122:125], v[134:137], v[38:41]
	s_waitcnt lgkmcnt(4)
	v_mfma_f32_16x16x32_f16 v[66:69], v[118:121], v[138:141], v[66:69]
	v_mfma_f32_16x16x32_f16 v[34:37], v[122:125], v[138:141], v[34:37]
	s_waitcnt lgkmcnt(3)
	v_mfma_f32_16x16x32_f16 v[18:21], v[118:121], v[142:145], v[18:21]
	v_mfma_f32_16x16x32_f16 v[2:5], v[122:125], v[142:145], v[2:5]
	s_waitcnt lgkmcnt(2)
	v_mfma_f32_16x16x32_f16 v[26:29], v[118:121], v[146:149], v[26:29]
	v_mfma_f32_16x16x32_f16 v[10:13], v[122:125], v[146:149], v[10:13]
	s_waitcnt lgkmcnt(1)
	v_mfma_f32_16x16x32_f16 v[22:25], v[118:121], v[150:153], v[22:25]
	v_mfma_f32_16x16x32_f16 v[6:9], v[122:125], v[150:153], v[6:9]
	s_waitcnt lgkmcnt(0)
	v_mfma_f32_16x16x32_f16 v[30:33], v[118:121], v[154:157], v[30:33]
	v_mfma_f32_16x16x32_f16 v[14:17], v[122:125], v[154:157], v[14:17]
	s_waitcnt vmcnt(0)
	s_barrier
	ds_read_b128 v[110:113], v158 offset:0
	ds_read_b128 v[114:117], v158 offset:2048
	ds_read_b128 v[118:121], v159 offset:0
	ds_read_b128 v[122:125], v159 offset:2048
	ds_read_b128 v[126:129], v160 offset:16384
	ds_read_b128 v[130:133], v160 offset:18432
	ds_read_b128 v[134:137], v160 offset:20480
	ds_read_b128 v[138:141], v160 offset:22528
	ds_read_b128 v[142:145], v160 offset:24576
	ds_read_b128 v[146:149], v160 offset:26624
	ds_read_b128 v[150:153], v160 offset:28672
	ds_read_b128 v[154:157], v160 offset:30720
	s_waitcnt lgkmcnt(7)
	v_mfma_f32_16x16x32_f16 v[164:167], v[110:113], v[126:129], v[164:167]
	v_mfma_f32_16x16x32_f16 v[62:65], v[114:117], v[126:129], v[62:65]
	ds_read_b128 v[126:129], v160 offset:32768
	s_waitcnt lgkmcnt(7)
	v_mfma_f32_16x16x32_f16 v[86:89], v[110:113], v[130:133], v[86:89]
	v_mfma_f32_16x16x32_f16 v[58:61], v[114:117], v[130:133], v[58:61]
	ds_read_b128 v[130:133], v160 offset:34816
	s_waitcnt lgkmcnt(7)
	v_mfma_f32_16x16x32_f16 v[96:99], v[110:113], v[134:137], v[96:99]
	v_mfma_f32_16x16x32_f16 v[54:57], v[114:117], v[134:137], v[54:57]
	ds_read_b128 v[134:137], v160 offset:36864
	s_waitcnt lgkmcnt(7)
	v_mfma_f32_16x16x32_f16 v[82:85], v[110:113], v[138:141], v[82:85]
	v_mfma_f32_16x16x32_f16 v[50:53], v[114:117], v[138:141], v[50:53]
	ds_read_b128 v[138:141], v160 offset:38912
	s_waitcnt lgkmcnt(7)
	v_mfma_f32_16x16x32_f16 v[78:81], v[110:113], v[142:145], v[78:81]
	v_mfma_f32_16x16x32_f16 v[46:49], v[114:117], v[142:145], v[46:49]
	ds_read_b128 v[142:145], v161 offset:16384
	s_waitcnt lgkmcnt(7)
	v_mfma_f32_16x16x32_f16 v[74:77], v[110:113], v[146:149], v[74:77]
	v_mfma_f32_16x16x32_f16 v[42:45], v[114:117], v[146:149], v[42:45]
	ds_read_b128 v[146:149], v161 offset:18432
	s_waitcnt lgkmcnt(7)
	v_mfma_f32_16x16x32_f16 v[70:73], v[110:113], v[150:153], v[70:73]
	v_mfma_f32_16x16x32_f16 v[38:41], v[114:117], v[150:153], v[38:41]
	ds_read_b128 v[150:153], v161 offset:20480
	s_waitcnt lgkmcnt(7)
	v_mfma_f32_16x16x32_f16 v[66:69], v[110:113], v[154:157], v[66:69]
	v_mfma_f32_16x16x32_f16 v[34:37], v[114:117], v[154:157], v[34:37]
	ds_read_b128 v[154:157], v161 offset:22528
	s_waitcnt lgkmcnt(7)
	v_mfma_f32_16x16x32_f16 v[18:21], v[110:113], v[126:129], v[18:21]
	v_mfma_f32_16x16x32_f16 v[2:5], v[114:117], v[126:129], v[2:5]
	ds_read_b128 v[126:129], v161 offset:24576
	s_waitcnt lgkmcnt(7)
	v_mfma_f32_16x16x32_f16 v[26:29], v[110:113], v[130:133], v[26:29]
	v_mfma_f32_16x16x32_f16 v[10:13], v[114:117], v[130:133], v[10:13]
	ds_read_b128 v[130:133], v161 offset:26624
	s_waitcnt lgkmcnt(7)
	v_mfma_f32_16x16x32_f16 v[22:25], v[110:113], v[134:137], v[22:25]
	v_mfma_f32_16x16x32_f16 v[6:9], v[114:117], v[134:137], v[6:9]
	ds_read_b128 v[134:137], v161 offset:28672
	s_waitcnt lgkmcnt(7)
	v_mfma_f32_16x16x32_f16 v[30:33], v[110:113], v[138:141], v[30:33]
	v_mfma_f32_16x16x32_f16 v[14:17], v[114:117], v[138:141], v[14:17]
	ds_read_b128 v[138:141], v161 offset:30720
	s_waitcnt lgkmcnt(7)
	v_mfma_f32_16x16x32_f16 v[164:167], v[118:121], v[142:145], v[164:167]
	v_mfma_f32_16x16x32_f16 v[62:65], v[122:125], v[142:145], v[62:65]
	ds_read_b128 v[142:145], v161 offset:32768
	s_waitcnt lgkmcnt(7)
	v_mfma_f32_16x16x32_f16 v[86:89], v[118:121], v[146:149], v[86:89]
	v_mfma_f32_16x16x32_f16 v[58:61], v[122:125], v[146:149], v[58:61]
	ds_read_b128 v[146:149], v161 offset:34816
	s_waitcnt lgkmcnt(7)
	v_mfma_f32_16x16x32_f16 v[96:99], v[118:121], v[150:153], v[96:99]
	v_mfma_f32_16x16x32_f16 v[54:57], v[122:125], v[150:153], v[54:57]
	ds_read_b128 v[150:153], v161 offset:36864
	s_waitcnt lgkmcnt(7)
	v_mfma_f32_16x16x32_f16 v[82:85], v[118:121], v[154:157], v[82:85]
	v_mfma_f32_16x16x32_f16 v[50:53], v[122:125], v[154:157], v[50:53]
	ds_read_b128 v[154:157], v161 offset:38912
	s_waitcnt lgkmcnt(0)
	s_barrier
	s_waitcnt lgkmcnt(7)
	v_mfma_f32_16x16x32_f16 v[78:81], v[118:121], v[126:129], v[78:81]
	v_mfma_f32_16x16x32_f16 v[46:49], v[122:125], v[126:129], v[46:49]
	s_waitcnt lgkmcnt(6)
	v_mfma_f32_16x16x32_f16 v[74:77], v[118:121], v[130:133], v[74:77]
	v_mfma_f32_16x16x32_f16 v[42:45], v[122:125], v[130:133], v[42:45]
	s_waitcnt lgkmcnt(5)
	v_mfma_f32_16x16x32_f16 v[70:73], v[118:121], v[134:137], v[70:73]
	v_mfma_f32_16x16x32_f16 v[38:41], v[122:125], v[134:137], v[38:41]
	s_waitcnt lgkmcnt(4)
	v_mfma_f32_16x16x32_f16 v[66:69], v[118:121], v[138:141], v[66:69]
	v_mfma_f32_16x16x32_f16 v[34:37], v[122:125], v[138:141], v[34:37]
	s_waitcnt lgkmcnt(3)
	v_mfma_f32_16x16x32_f16 v[18:21], v[118:121], v[142:145], v[18:21]
	v_mfma_f32_16x16x32_f16 v[2:5], v[122:125], v[142:145], v[2:5]
	s_waitcnt lgkmcnt(2)
	v_mfma_f32_16x16x32_f16 v[26:29], v[118:121], v[146:149], v[26:29]
	v_mfma_f32_16x16x32_f16 v[10:13], v[122:125], v[146:149], v[10:13]
	s_waitcnt lgkmcnt(1)
	v_mfma_f32_16x16x32_f16 v[22:25], v[118:121], v[150:153], v[22:25]
	v_mfma_f32_16x16x32_f16 v[6:9], v[122:125], v[150:153], v[6:9]
	s_waitcnt lgkmcnt(0)
	v_mfma_f32_16x16x32_f16 v[30:33], v[118:121], v[154:157], v[30:33]
	v_mfma_f32_16x16x32_f16 v[14:17], v[122:125], v[154:157], v[14:17]
	s_nop 15
	s_nop 15
	s_movk_i32 s2, 0xfc
	v_cmp_gt_u32_e32 vcc, s2, v0
	s_mov_b32 s2, 0x12492493
	s_movk_i32 s4, 0x380
	s_movk_i32 s12, 0x110
	v_cmp_gt_u32_e64 s[4:5], s4, v0
	v_lshrrev_b32_e32 v93, 1, v0
	v_cndmask_b32_e32 v94, 0, v93, vcc
	s_nop 5
	v_cvt_f16_f32_e32 v86, v86
	s_nop 5
	v_cvt_f16_f32_e32 v54, v54
	v_cvt_f16_f32_e32 v82, v82
	v_cvt_f16_f32_e32 v50, v50
	s_nop 5
	v_cvt_f16_f32_e32 v78, v78
	v_mul_i32_i24_e32 v102, 0xffffffc2, v92
	v_mul_u32_u24_e32 v101, 0x110, v91
	v_lshlrev_b32_e32 v91, 6, v92
	v_add3_u32 v91, v91, v102, v101
	ds_write_b16 v91, v86 offset:32
	v_cvt_f16_f32_e32 v86, v87
	v_cvt_f16_f32_e32 v74, v74
	v_cvt_f16_f32_e32 v102, v165
	ds_write_b16 v91, v86 offset:304
	v_cvt_f16_f32_e32 v86, v88
	s_nop 2
	v_cvt_f16_f32_e32 v34, v34
	ds_write_b16 v91, v82 offset:96
	ds_write_b16 v91, v86 offset:576
	v_cvt_f16_f32_e32 v86, v89
	v_cvt_f16_f32_e32 v38, v38
	ds_write_b16 v91, v34 offset:4576
	ds_write_b16 v91, v86 offset:848
	v_cvt_f16_f32_e32 v86, v96
	s_nop 1
	v_cvt_f16_f32_e32 v62, v62
	v_cvt_f16_f32_e32 v34, v35
	s_nop 0
	v_cvt_f16_f32_e32 v58, v58
	ds_write_b16 v91, v38 offset:4544
	v_cvt_f16_f32_e32 v38, v39
	s_nop 1
	v_cvt_f16_f32_e32 v46, v46
	ds_write_b16 v91, v86 offset:64
	v_cvt_f16_f32_e32 v86, v97
	s_nop 0
	v_cvt_f16_f32_e32 v42, v42
	v_cvt_f16_f32_e32 v82, v83
	ds_write_b16 v91, v78 offset:128
	s_nop 1
	v_cvt_f16_f32_e32 v70, v70
	v_cvt_f16_f32_e32 v78, v79
	ds_write_b16 v91, v74 offset:160
	v_cvt_f16_f32_e32 v74, v75
	s_nop 0
	v_cvt_f16_f32_e32 v66, v66
	ds_write_b16 v91, v70 offset:192
	v_cvt_f16_f32_e32 v70, v71
	ds_write_b16 v91, v62 offset:4352
	ds_write_b16 v91, v66 offset:224
	v_cvt_f16_f32_e32 v66, v67
	v_cvt_f16_f32_e32 v62, v63
	ds_write_b16 v91, v58 offset:4384
	v_cvt_f16_f32_e32 v58, v59
	ds_write_b16 v91, v54 offset:4416
	v_cvt_f16_f32_e32 v54, v55
	ds_write_b16 v91, v50 offset:4448
	v_cvt_f16_f32_e32 v50, v51
	ds_write_b16 v91, v46 offset:4480
	v_cvt_f16_f32_e32 v46, v47
	ds_write_b16 v91, v42 offset:4512
	v_cvt_f16_f32_e32 v42, v43
	ds_write_b16 v91, v34 offset:4848
	v_cvt_f16_f32_e32 v34, v36
	ds_write_b16 v91, v38 offset:4816
	v_cvt_f16_f32_e32 v38, v40
	ds_write_b16 v91, v102 offset:272
	v_cvt_f16_f32_e32 v102, v166
	ds_write_b16 v91, v86 offset:336
	v_cvt_f16_f32_e32 v86, v98
	ds_write_b16 v91, v82 offset:368
	v_cvt_f16_f32_e32 v82, v84
	ds_write_b16 v91, v78 offset:400
	v_cvt_f16_f32_e32 v78, v80
	ds_write_b16 v91, v74 offset:432
	v_cvt_f16_f32_e32 v74, v76
	ds_write_b16 v91, v70 offset:464
	v_cvt_f16_f32_e32 v70, v72
	ds_write_b16 v91, v66 offset:496
	v_cvt_f16_f32_e32 v66, v68
	ds_write_b16 v91, v62 offset:4624
	v_cvt_f16_f32_e32 v62, v64
	ds_write_b16 v91, v58 offset:4656
	v_cvt_f16_f32_e32 v58, v60
	ds_write_b16 v91, v54 offset:4688
	v_cvt_f16_f32_e32 v54, v56
	ds_write_b16 v91, v50 offset:4720
	v_cvt_f16_f32_e32 v50, v52
	ds_write_b16 v91, v46 offset:4752
	v_cvt_f16_f32_e32 v46, v48
	ds_write_b16 v91, v42 offset:4784
	v_cvt_f16_f32_e32 v42, v44
	ds_write_b16 v91, v34 offset:5120
	v_cvt_f16_f32_e32 v34, v37
	ds_write_b16 v91, v38 offset:5088
	v_cvt_f16_f32_e32 v38, v41
	v_cvt_f16_f32_e32 v103, v164
	ds_write_b16 v91, v102 offset:544
	v_cvt_f16_f32_e32 v102, v167
	ds_write_b16 v91, v86 offset:608
	v_cvt_f16_f32_e32 v86, v99
	ds_write_b16 v91, v82 offset:640
	v_cvt_f16_f32_e32 v82, v85
	ds_write_b16 v91, v78 offset:672
	v_cvt_f16_f32_e32 v78, v81
	ds_write_b16 v91, v74 offset:704
	v_cvt_f16_f32_e32 v74, v77
	ds_write_b16 v91, v70 offset:736
	v_cvt_f16_f32_e32 v70, v73
	ds_write_b16 v91, v66 offset:768
	v_cvt_f16_f32_e32 v66, v69
	ds_write_b16 v91, v62 offset:4896
	v_cvt_f16_f32_e32 v62, v65
	ds_write_b16 v91, v58 offset:4928
	v_cvt_f16_f32_e32 v58, v61
	ds_write_b16 v91, v54 offset:4960
	v_cvt_f16_f32_e32 v54, v57
	ds_write_b16 v91, v50 offset:4992
	v_cvt_f16_f32_e32 v50, v53
	ds_write_b16 v91, v46 offset:5024
	v_cvt_f16_f32_e32 v46, v49
	ds_write_b16 v91, v42 offset:5056
	v_cvt_f16_f32_e32 v42, v45
	ds_write_b16 v91, v34 offset:5392
	v_min_u32_e32 v34, 8, v92
	v_mul_hi_u32 v100, v94, s2
	ds_write_b16 v91, v38 offset:5360
	v_cmp_gt_u32_e64 s[2:3], 9, v92
	v_mul_u32_u24_e32 v39, 14, v34
	v_and_b32_e32 v40, 48, v0
	v_lshlrev_b32_e32 v38, 2, v92
	ds_write_b16 v91, v103
	ds_write_b16 v91, v102 offset:816
	ds_write_b16 v91, v86 offset:880
	ds_write_b16 v91, v82 offset:912
	ds_write_b16 v91, v78 offset:944
	ds_write_b16 v91, v74 offset:976
	ds_write_b16 v91, v70 offset:1008
	ds_write_b16 v91, v66 offset:1040
	ds_write_b16 v91, v62 offset:5168
	ds_write_b16 v91, v58 offset:5200
	ds_write_b16 v91, v54 offset:5232
	ds_write_b16 v91, v50 offset:5264
	ds_write_b16 v91, v46 offset:5296
	ds_write_b16 v91, v42 offset:5328
	s_waitcnt lgkmcnt(0)
	s_barrier
	s_and_saveexec_b64 s[6:7], s[4:5]
	s_cbranch_execz .LBB1_9
	v_add_u32_e32 v34, v1, v39
	v_mad_u32_u24 v41, v34, s12, v40
	ds_read_b128 v[34:37], v41
	ds_read_b128 v[42:45], v41 offset:64
	ds_read_b128 v[46:49], v41 offset:128
	ds_read_b128 v[50:53], v41 offset:192
	v_cmp_ne_u32_e64 s[4:5], 3, v90
	v_mul_u32_u24_e32 v41, 9, v1
	s_and_b64 s[12:13], s[4:5], s[2:3]
	s_waitcnt lgkmcnt(1)
	v_mfma_f32_16x16x32_f16 v[34:37], v[34:37], v[46:49], 0
	s_waitcnt lgkmcnt(0)
	v_mfma_f32_16x16x32_f16 v[34:37], v[42:45], v[50:53], v[34:37]
	s_and_saveexec_b64 s[4:5], s[12:13]
	v_add_u32_e32 v42, v95, v41
	s_nop 5
	v_mul_f32_e32 v34, 0x3e000000, v34
	v_mad_u32_u24 v42, v42, 48, v38
	ds_write_b32 v42, v34 offset:35328
	s_or_b64 exec, exec, s[4:5]
	v_or_b32_e32 v34, 1, v95
	v_cmp_gt_u32_e64 s[4:5], 9, v34
	s_and_b64 s[12:13], s[4:5], s[2:3]
	s_and_saveexec_b64 s[4:5], s[12:13]
	v_add_u32_e32 v34, v34, v41
	v_mul_f32_e32 v35, 0x3e000000, v35
	v_mad_u32_u24 v34, v34, 48, v38
	ds_write_b32 v34, v35 offset:35328
	s_or_b64 exec, exec, s[4:5]
	v_or_b32_e32 v34, 2, v95
	v_cmp_gt_u32_e64 s[4:5], 9, v34
	s_and_b64 s[12:13], s[4:5], s[2:3]
	s_and_saveexec_b64 s[4:5], s[12:13]
	v_add_u32_e32 v34, v34, v41
	v_mul_f32_e32 v35, 0x3e000000, v36
	v_mad_u32_u24 v34, v34, 48, v38
	ds_write_b32 v34, v35 offset:35328
	s_or_b64 exec, exec, s[4:5]
	v_or_b32_e32 v34, 3, v95
	v_cmp_gt_u32_e64 s[4:5], 9, v34
	s_and_b64 s[4:5], s[4:5], s[2:3]
	s_and_b64 exec, exec, s[4:5]
	v_add_u32_e32 v34, v34, v41
	v_mul_f32_e32 v35, 0x3e000000, v37
	v_mad_u32_u24 v34, v34, 48, v38
	ds_write_b32 v34, v35 offset:35328

.LBB2_30:
	s_or_b64 exec, exec, s[0:1]
	s_waitcnt lgkmcnt(0)
	s_barrier
	ds_read_b64 v[2:3], v83 offset:7848
	s_waitcnt lgkmcnt(0)
	v_cmp_eq_u32_e32 vcc, 0, v3
	v_readfirstlane_b32 s81, v2
	s_cbranch_vccnz .LBB2_3
	v_add_u32_e32 v2, s58, v127
	v_ashrrev_i32_e32 v3, 31, v2
	v_lshlrev_b64 v[4:5], 11, v[2:3]
	v_lshl_add_u64 v[4:5], v[86:87], 0, v[4:5]
	v_lshl_add_u64 v[2:3], v[2:3], 2, s[24:25]
	global_load_dword v6, v[2:3], off
	global_load_dwordx4 v[8:11], v[110:111], off
	global_load_dwordx4 v[12:15], v[4:5], off
	global_load_dwordx4 v[16:19], v[110:111], off offset:64
	global_load_dwordx4 v[20:23], v[4:5], off offset:64
	global_load_dwordx4 v[24:27], v[110:111], off offset:128
	global_load_dwordx4 v[28:31], v[4:5], off offset:128
	global_load_dwordx4 v[32:35], v[110:111], off offset:192
	global_load_dwordx4 v[36:39], v[4:5], off offset:192
	global_load_dwordx4 v[40:43], v[110:111], off offset:256
	global_load_dwordx4 v[44:47], v[4:5], off offset:256
	global_load_dwordx4 v[48:51], v[110:111], off offset:320
	global_load_dwordx4 v[52:55], v[4:5], off offset:320
	global_load_dwordx4 v[56:59], v[110:111], off offset:384
	global_load_dwordx4 v[60:63], v[4:5], off offset:384
	global_load_dwordx4 v[64:67], v[110:111], off offset:448
	global_load_dwordx4 v[68:71], v[4:5], off offset:448
	s_waitcnt vmcnt(14)
	v_mfma_f32_16x16x4_f32 a[0:3], v8, v12, 0
	v_mfma_f32_16x16x4_f32 a[4:7], v9, v13, 0
	v_mfma_f32_16x16x4_f32 a[0:3], v10, v14, a[0:3]
	v_mfma_f32_16x16x4_f32 a[4:7], v11, v15, a[4:7]
	global_load_dwordx4 v[8:11], v[110:111], off offset:512
	global_load_dwordx4 v[12:15], v[4:5], off offset:512
	s_waitcnt vmcnt(14)
	v_mfma_f32_16x16x4_f32 a[0:3], v16, v20, a[0:3]
	v_mfma_f32_16x16x4_f32 a[4:7], v17, v21, a[4:7]
	v_mfma_f32_16x16x4_f32 a[0:3], v18, v22, a[0:3]
	v_mfma_f32_16x16x4_f32 a[4:7], v19, v23, a[4:7]
	global_load_dwordx4 v[16:19], v[110:111], off offset:576
	global_load_dwordx4 v[20:23], v[4:5], off offset:576
	s_waitcnt vmcnt(14)
	v_mfma_f32_16x16x4_f32 a[0:3], v24, v28, a[0:3]
	v_mfma_f32_16x16x4_f32 a[4:7], v25, v29, a[4:7]
	v_mfma_f32_16x16x4_f32 a[0:3], v26, v30, a[0:3]
	v_mfma_f32_16x16x4_f32 a[4:7], v27, v31, a[4:7]
	global_load_dwordx4 v[24:27], v[110:111], off offset:640
	global_load_dwordx4 v[28:31], v[4:5], off offset:640
	s_waitcnt vmcnt(14)
	v_mfma_f32_16x16x4_f32 a[0:3], v32, v36, a[0:3]
	v_mfma_f32_16x16x4_f32 a[4:7], v33, v37, a[4:7]
	v_mfma_f32_16x16x4_f32 a[0:3], v34, v38, a[0:3]
	v_mfma_f32_16x16x4_f32 a[4:7], v35, v39, a[4:7]
	global_load_dwordx4 v[32:35], v[110:111], off offset:704
	global_load_dwordx4 v[36:39], v[4:5], off offset:704
	s_waitcnt vmcnt(14)
	v_mfma_f32_16x16x4_f32 a[0:3], v40, v44, a[0:3]
	v_mfma_f32_16x16x4_f32 a[4:7], v41, v45, a[4:7]
	v_mfma_f32_16x16x4_f32 a[0:3], v42, v46, a[0:3]
	v_mfma_f32_16x16x4_f32 a[4:7], v43, v47, a[4:7]
	global_load_dwordx4 v[40:43], v[110:111], off offset:768
	global_load_dwordx4 v[44:47], v[4:5], off offset:768
	s_waitcnt vmcnt(14)
	v_mfma_f32_16x16x4_f32 a[0:3], v48, v52, a[0:3]
	v_mfma_f32_16x16x4_f32 a[4:7], v49, v53, a[4:7]
	v_mfma_f32_16x16x4_f32 a[0:3], v50, v54, a[0:3]
	v_mfma_f32_16x16x4_f32 a[4:7], v51, v55, a[4:7]
	global_load_dwordx4 v[48:51], v[110:111], off offset:832
	global_load_dwordx4 v[52:55], v[4:5], off offset:832
	s_waitcnt vmcnt(14)
	v_mfma_f32_16x16x4_f32 a[0:3], v56, v60, a[0:3]
	v_mfma_f32_16x16x4_f32 a[4:7], v57, v61, a[4:7]
	v_mfma_f32_16x16x4_f32 a[0:3], v58, v62, a[0:3]
	v_mfma_f32_16x16x4_f32 a[4:7], v59, v63, a[4:7]
	global_load_dwordx4 v[56:59], v[110:111], off offset:896
	global_load_dwordx4 v[60:63], v[4:5], off offset:896
	s_waitcnt vmcnt(14)
	v_mfma_f32_16x16x4_f32 a[0:3], v64, v68, a[0:3]
	v_mfma_f32_16x16x4_f32 a[4:7], v65, v69, a[4:7]
	v_mfma_f32_16x16x4_f32 a[0:3], v66, v70, a[0:3]
	v_mfma_f32_16x16x4_f32 a[4:7], v67, v71, a[4:7]
	global_load_dwordx4 v[64:67], v[110:111], off offset:960
	global_load_dwordx4 v[68:71], v[4:5], off offset:960
	s_waitcnt vmcnt(14)
	v_mfma_f32_16x16x4_f32 a[0:3], v8, v12, a[0:3]
	v_mfma_f32_16x16x4_f32 a[4:7], v9, v13, a[4:7]
	v_mfma_f32_16x16x4_f32 a[0:3], v10, v14, a[0:3]
	v_mfma_f32_16x16x4_f32 a[4:7], v11, v15, a[4:7]
	global_load_dwordx4 v[8:11], v[110:111], off offset:1024
	global_load_dwordx4 v[12:15], v[4:5], off offset:1024
	s_waitcnt vmcnt(14)
	v_mfma_f32_16x16x4_f32 a[0:3], v16, v20, a[0:3]
	v_mfma_f32_16x16x4_f32 a[4:7], v17, v21, a[4:7]
	v_mfma_f32_16x16x4_f32 a[0:3], v18, v22, a[0:3]
	v_mfma_f32_16x16x4_f32 a[4:7], v19, v23, a[4:7]
	global_load_dwordx4 v[16:19], v[110:111], off offset:1088
	global_load_dwordx4 v[20:23], v[4:5], off offset:1088
	s_waitcnt vmcnt(14)
	v_mfma_f32_16x16x4_f32 a[0:3], v24, v28, a[0:3]
	v_mfma_f32_16x16x4_f32 a[4:7], v25, v29, a[4:7]
	v_mfma_f32_16x16x4_f32 a[0:3], v26, v30, a[0:3]
	v_mfma_f32_16x16x4_f32 a[4:7], v27, v31, a[4:7]
	global_load_dwordx4 v[24:27], v[110:111], off offset:1152
	global_load_dwordx4 v[28:31], v[4:5], off offset:1152
	s_waitcnt vmcnt(14)
	v_mfma_f32_16x16x4_f32 a[0:3], v32, v36, a[0:3]
	v_mfma_f32_16x16x4_f32 a[4:7], v33, v37, a[4:7]
	v_mfma_f32_16x16x4_f32 a[0:3], v34, v38, a[0:3]
	v_mfma_f32_16x16x4_f32 a[4:7], v35, v39, a[4:7]
	global_load_dwordx4 v[32:35], v[110:111], off offset:1216
	global_load_dwordx4 v[36:39], v[4:5], off offset:1216
	s_waitcnt vmcnt(14)
	v_mfma_f32_16x16x4_f32 a[0:3], v40, v44, a[0:3]
	v_mfma_f32_16x16x4_f32 a[4:7], v41, v45, a[4:7]
	v_mfma_f32_16x16x4_f32 a[0:3], v42, v46, a[0:3]
	v_mfma_f32_16x16x4_f32 a[4:7], v43, v47, a[4:7]
	global_load_dwordx4 v[40:43], v[110:111], off offset:1280
	global_load_dwordx4 v[44:47], v[4:5], off offset:1280
	s_waitcnt vmcnt(14)
	v_mfma_f32_16x16x4_f32 a[0:3], v48, v52, a[0:3]
	v_mfma_f32_16x16x4_f32 a[4:7], v49, v53, a[4:7]
	v_mfma_f32_16x16x4_f32 a[0:3], v50, v54, a[0:3]
	v_mfma_f32_16x16x4_f32 a[4:7], v51, v55, a[4:7]
	global_load_dwordx4 v[48:51], v[110:111], off offset:1344
	global_load_dwordx4 v[52:55], v[4:5], off offset:1344
	s_waitcnt vmcnt(14)
	v_mfma_f32_16x16x4_f32 a[0:3], v56, v60, a[0:3]
	v_mfma_f32_16x16x4_f32 a[4:7], v57, v61, a[4:7]
	v_mfma_f32_16x16x4_f32 a[0:3], v58, v62, a[0:3]
	v_mfma_f32_16x16x4_f32 a[4:7], v59, v63, a[4:7]
	global_load_dwordx4 v[56:59], v[110:111], off offset:1408
	global_load_dwordx4 v[60:63], v[4:5], off offset:1408
	s_waitcnt vmcnt(14)
	v_mfma_f32_16x16x4_f32 a[0:3], v64, v68, a[0:3]
	v_mfma_f32_16x16x4_f32 a[4:7], v65, v69, a[4:7]
	v_mfma_f32_16x16x4_f32 a[0:3], v66, v70, a[0:3]
	v_mfma_f32_16x16x4_f32 a[4:7], v67, v71, a[4:7]
	global_load_dwordx4 v[64:67], v[110:111], off offset:1472
	global_load_dwordx4 v[68:71], v[4:5], off offset:1472
	s_waitcnt vmcnt(14)
	v_mfma_f32_16x16x4_f32 a[0:3], v8, v12, a[0:3]
	v_mfma_f32_16x16x4_f32 a[4:7], v9, v13, a[4:7]
	v_mfma_f32_16x16x4_f32 a[0:3], v10, v14, a[0:3]
	v_mfma_f32_16x16x4_f32 a[4:7], v11, v15, a[4:7]
	global_load_dwordx4 v[8:11], v[110:111], off offset:1536
	global_load_dwordx4 v[12:15], v[4:5], off offset:1536
	s_waitcnt vmcnt(14)
	v_mfma_f32_16x16x4_f32 a[0:3], v16, v20, a[0:3]
	v_mfma_f32_16x16x4_f32 a[4:7], v17, v21, a[4:7]
	v_mfma_f32_16x16x4_f32 a[0:3], v18, v22, a[0:3]
	v_mfma_f32_16x16x4_f32 a[4:7], v19, v23, a[4:7]
	global_load_dwordx4 v[16:19], v[110:111], off offset:1600
	global_load_dwordx4 v[20:23], v[4:5], off offset:1600
	s_waitcnt vmcnt(14)
	v_mfma_f32_16x16x4_f32 a[0:3], v24, v28, a[0:3]
	v_mfma_f32_16x16x4_f32 a[4:7], v25, v29, a[4:7]
	v_mfma_f32_16x16x4_f32 a[0:3], v26, v30, a[0:3]
	v_mfma_f32_16x16x4_f32 a[4:7], v27, v31, a[4:7]
	global_load_dwordx4 v[24:27], v[110:111], off offset:1664
	global_load_dwordx4 v[28:31], v[4:5], off offset:1664
	s_waitcnt vmcnt(14)
	v_mfma_f32_16x16x4_f32 a[0:3], v32, v36, a[0:3]
	v_mfma_f32_16x16x4_f32 a[4:7], v33, v37, a[4:7]
	v_mfma_f32_16x16x4_f32 a[0:3], v34, v38, a[0:3]
	v_mfma_f32_16x16x4_f32 a[4:7], v35, v39, a[4:7]
	global_load_dwordx4 v[32:35], v[110:111], off offset:1728
	global_load_dwordx4 v[36:39], v[4:5], off offset:1728
	s_waitcnt vmcnt(14)
	v_mfma_f32_16x16x4_f32 a[0:3], v40, v44, a[0:3]
	v_mfma_f32_16x16x4_f32 a[4:7], v41, v45, a[4:7]
	v_mfma_f32_16x16x4_f32 a[0:3], v42, v46, a[0:3]
	v_mfma_f32_16x16x4_f32 a[4:7], v43, v47, a[4:7]
	global_load_dwordx4 v[40:43], v[110:111], off offset:1792
	global_load_dwordx4 v[44:47], v[4:5], off offset:1792
	s_waitcnt vmcnt(14)
	v_mfma_f32_16x16x4_f32 a[0:3], v48, v52, a[0:3]
	v_mfma_f32_16x16x4_f32 a[4:7], v49, v53, a[4:7]
	v_mfma_f32_16x16x4_f32 a[0:3], v50, v54, a[0:3]
	v_mfma_f32_16x16x4_f32 a[4:7], v51, v55, a[4:7]
	global_load_dwordx4 v[48:51], v[110:111], off offset:1856
	global_load_dwordx4 v[52:55], v[4:5], off offset:1856
	s_waitcnt vmcnt(14)
	v_mfma_f32_16x16x4_f32 a[0:3], v56, v60, a[0:3]
	v_mfma_f32_16x16x4_f32 a[4:7], v57, v61, a[4:7]
	v_mfma_f32_16x16x4_f32 a[0:3], v58, v62, a[0:3]
	v_mfma_f32_16x16x4_f32 a[4:7], v59, v63, a[4:7]
	global_load_dwordx4 v[56:59], v[110:111], off offset:1920
	global_load_dwordx4 v[60:63], v[4:5], off offset:1920
	s_waitcnt vmcnt(14)
	v_mfma_f32_16x16x4_f32 a[0:3], v64, v68, a[0:3]
	v_mfma_f32_16x16x4_f32 a[4:7], v65, v69, a[4:7]
	v_mfma_f32_16x16x4_f32 a[0:3], v66, v70, a[0:3]
	v_mfma_f32_16x16x4_f32 a[4:7], v67, v71, a[4:7]
	global_load_dwordx4 v[64:67], v[110:111], off offset:1984
	global_load_dwordx4 v[68:71], v[4:5], off offset:1984
	s_waitcnt vmcnt(14)
	v_mfma_f32_16x16x4_f32 a[0:3], v8, v12, a[0:3]
	v_mfma_f32_16x16x4_f32 a[4:7], v9, v13, a[4:7]
	v_mfma_f32_16x16x4_f32 a[0:3], v10, v14, a[0:3]
	v_mfma_f32_16x16x4_f32 a[4:7], v11, v15, a[4:7]
	s_waitcnt vmcnt(12)
	v_mfma_f32_16x16x4_f32 a[0:3], v16, v20, a[0:3]
	v_mfma_f32_16x16x4_f32 a[4:7], v17, v21, a[4:7]
	v_mfma_f32_16x16x4_f32 a[0:3], v18, v22, a[0:3]
	v_mfma_f32_16x16x4_f32 a[4:7], v19, v23, a[4:7]
	s_waitcnt vmcnt(10)
	v_mfma_f32_16x16x4_f32 a[0:3], v24, v28, a[0:3]
	v_mfma_f32_16x16x4_f32 a[4:7], v25, v29, a[4:7]
	v_mfma_f32_16x16x4_f32 a[0:3], v26, v30, a[0:3]
	v_mfma_f32_16x16x4_f32 a[4:7], v27, v31, a[4:7]
	s_waitcnt vmcnt(8)
	v_mfma_f32_16x16x4_f32 a[0:3], v32, v36, a[0:3]
	v_mfma_f32_16x16x4_f32 a[4:7], v33, v37, a[4:7]
	v_mfma_f32_16x16x4_f32 a[0:3], v34, v38, a[0:3]
	v_mfma_f32_16x16x4_f32 a[4:7], v35, v39, a[4:7]
	s_waitcnt vmcnt(6)
	v_mfma_f32_16x16x4_f32 a[0:3], v40, v44, a[0:3]
	v_mfma_f32_16x16x4_f32 a[4:7], v41, v45, a[4:7]
	v_mfma_f32_16x16x4_f32 a[0:3], v42, v46, a[0:3]
	v_mfma_f32_16x16x4_f32 a[4:7], v43, v47, a[4:7]
	s_waitcnt vmcnt(4)
	v_mfma_f32_16x16x4_f32 a[0:3], v48, v52, a[0:3]
	v_mfma_f32_16x16x4_f32 a[4:7], v49, v53, a[4:7]
	v_mfma_f32_16x16x4_f32 a[0:3], v50, v54, a[0:3]
	v_mfma_f32_16x16x4_f32 a[4:7], v51, v55, a[4:7]
	s_waitcnt vmcnt(2)
	v_mfma_f32_16x16x4_f32 a[0:3], v56, v60, a[0:3]
	v_mfma_f32_16x16x4_f32 a[4:7], v57, v61, a[4:7]
	v_mfma_f32_16x16x4_f32 a[0:3], v58, v62, a[0:3]
	v_mfma_f32_16x16x4_f32 a[4:7], v59, v63, a[4:7]
	s_waitcnt vmcnt(0)
	v_mfma_f32_16x16x4_f32 a[0:3], v64, v68, a[0:3]
	v_mfma_f32_16x16x4_f32 a[4:7], v65, v69, a[4:7]
	v_mfma_f32_16x16x4_f32 a[0:3], v66, v70, a[0:3]
	v_mfma_f32_16x16x4_f32 a[4:7], v67, v71, a[4:7]
	s_nop 15
	v_accvgpr_read_b32 v5, a3
	v_accvgpr_read_b32 v4, a2
	v_accvgpr_read_b32 v3, a1
	v_accvgpr_read_b32 v2, a0
	v_accvgpr_read_b32 v8, a4
	v_accvgpr_read_b32 v9, a5
	v_accvgpr_read_b32 v10, a6
	v_accvgpr_read_b32 v11, a7
	s_nop 1
	v_add_f32_e32 v2, v2, v8
	v_add_f32_e32 v3, v3, v9
	v_add_f32_e32 v4, v4, v10
	v_add_f32_e32 v5, v5, v11
	s_and_saveexec_b64 s[0:1], s[10:11]
	s_cbranch_execnz .LBB2_49
	s_or_b64 exec, exec, s[0:1]
	s_and_saveexec_b64 s[0:1], s[12:13]
	s_cbranch_execnz .LBB2_50
